# GEMM K-loops: setprio 1 before the phase barrier, redundant lgkmcnt waits behind it and mid-segment setprio 0/1 pairs removed, closing setprio 0 behind its barrier
# baseline (speedup 1.0000x reference)
.LBB0_341:
	ds_read_b128 v[120:123], v167
	ds_read_b128 v[124:127], v167 offset:1024
	ds_read_b128 v[128:131], v167 offset:2048
	ds_read_b128 v[132:135], v167 offset:3072
	ds_read_b128 v[160:163], v168
	ds_read_b128 v[170:173], v168 offset:1024
	ds_read_b128 v[174:177], v168 offset:2048
	ds_read_b128 v[178:181], v168 offset:3072
	s_add_u32 s38, s2, 0xfff80080
	s_addc_u32 s39, s3, -1
	s_cmp_eq_u32 s60, 4
	s_cselect_b32 s41, s31, s39
	s_cselect_b32 s40, s30, s38
	s_cselect_b32 s39, s35, s59
	s_cselect_b32 s38, s34, s29
	v_lshl_add_u64 v[164:165], s[2:3], 0, v[152:153]
	s_add_i32 m0, s37, 0xc000
	ds_read_b128 v[182:185], v169
	ds_read_b128 v[186:189], v169 offset:1024
	ds_read_b128 v[190:193], v169 offset:2048
	ds_read_b128 v[194:197], v169 offset:3072
	ds_read_b128 v[198:201], v169 offset:4096
	ds_read_b128 v[202:205], v169 offset:5120
	ds_read_b128 v[206:209], v169 offset:6144
	ds_read_b128 v[210:213], v169 offset:7168
	global_load_lds_dwordx4 v[164:165], off
	v_lshl_add_u64 v[164:165], s[2:3], 0, v[154:155]
	s_add_i32 m0, s37, 0xe000
	s_nop 0
	global_load_lds_dwordx4 v[164:165], off
	s_waitcnt vmcnt(8)
	s_waitcnt lgkmcnt(0)
	s_setprio 1
	s_barrier
	v_mfma_f32_16x16x32_bf16 v[140:143], v[120:123], v[182:185], v[140:143]
	v_mfma_f32_16x16x32_bf16 v[136:139], v[128:131], v[182:185], v[136:139]
	v_mfma_f32_16x16x32_bf16 v[108:111], v[120:123], v[190:193], v[108:111]
	v_mfma_f32_16x16x32_bf16 v[104:107], v[128:131], v[190:193], v[104:107]
	v_mfma_f32_16x16x32_bf16 v[92:95], v[120:123], v[198:201], v[92:95]
	v_mfma_f32_16x16x32_bf16 v[88:91], v[128:131], v[198:201], v[88:91]
	v_mfma_f32_16x16x32_bf16 v[76:79], v[120:123], v[206:209], v[76:79]
	v_mfma_f32_16x16x32_bf16 v[72:75], v[128:131], v[206:209], v[72:75]
	v_mfma_f32_16x16x32_bf16 v[140:143], v[124:127], v[186:189], v[140:143]
	v_mfma_f32_16x16x32_bf16 v[136:139], v[132:135], v[186:189], v[136:139]
	v_mfma_f32_16x16x32_bf16 v[108:111], v[124:127], v[194:197], v[108:111]
	v_mfma_f32_16x16x32_bf16 v[104:107], v[132:135], v[194:197], v[104:107]
	v_mfma_f32_16x16x32_bf16 v[92:95], v[124:127], v[202:205], v[92:95]
	v_mfma_f32_16x16x32_bf16 v[88:91], v[132:135], v[202:205], v[88:91]
	v_mfma_f32_16x16x32_bf16 v[76:79], v[124:127], v[210:213], v[76:79]
	v_mfma_f32_16x16x32_bf16 v[72:75], v[132:135], v[210:213], v[72:75]
	v_mfma_f32_16x16x32_bf16 v[116:119], v[160:163], v[182:185], v[116:119]
	v_mfma_f32_16x16x32_bf16 v[112:115], v[174:177], v[182:185], v[112:115]
	v_mfma_f32_16x16x32_bf16 v[100:103], v[160:163], v[190:193], v[100:103]
	v_mfma_f32_16x16x32_bf16 v[96:99], v[174:177], v[190:193], v[96:99]
	v_mfma_f32_16x16x32_bf16 v[84:87], v[160:163], v[198:201], v[84:87]
	v_mfma_f32_16x16x32_bf16 v[80:83], v[174:177], v[198:201], v[80:83]
	v_mfma_f32_16x16x32_bf16 v[68:71], v[160:163], v[206:209], v[68:71]
	v_mfma_f32_16x16x32_bf16 v[64:67], v[174:177], v[206:209], v[64:67]
	v_mfma_f32_16x16x32_bf16 v[116:119], v[170:173], v[186:189], v[116:119]
	v_mfma_f32_16x16x32_bf16 v[112:115], v[178:181], v[186:189], v[112:115]
	v_mfma_f32_16x16x32_bf16 v[100:103], v[170:173], v[194:197], v[100:103]
	v_mfma_f32_16x16x32_bf16 v[96:99], v[178:181], v[194:197], v[96:99]
	v_mfma_f32_16x16x32_bf16 v[84:87], v[170:173], v[202:205], v[84:87]
	v_mfma_f32_16x16x32_bf16 v[80:83], v[178:181], v[202:205], v[80:83]
	v_mfma_f32_16x16x32_bf16 v[68:71], v[170:173], v[210:213], v[68:71]
	v_mfma_f32_16x16x32_bf16 v[64:67], v[178:181], v[210:213], v[64:67]
	s_barrier
	s_setprio 0
	s_add_i32 s61, s55, s44
	v_lshl_add_u64 v[164:165], s[38:39], 0, v[148:149]
	s_mov_b32 m0, s61
	ds_read_b128 v[182:185], v169 offset:16384
	ds_read_b128 v[186:189], v169 offset:17408
	ds_read_b128 v[190:193], v169 offset:18432
	ds_read_b128 v[194:197], v169 offset:19456
	ds_read_b128 v[198:201], v169 offset:20480
	ds_read_b128 v[202:205], v169 offset:21504
	ds_read_b128 v[206:209], v169 offset:22528
	ds_read_b128 v[210:213], v169 offset:23552
	global_load_lds_dwordx4 v[164:165], off
	s_add_i32 m0, s61, 0x2000
	s_add_u32 s62, s38, 0x20000
	v_lshl_add_u64 v[214:215], s[38:39], 0, v[144:145]
	s_addc_u32 s63, s39, 0
	s_add_i32 s61, s56, s44
	global_load_lds_dwordx4 v[214:215], off
	v_lshl_add_u64 v[216:217], s[62:63], 0, v[148:149]
	s_mov_b32 m0, s61
	v_lshl_add_u64 v[218:219], s[40:41], 0, v[146:147]
	global_load_lds_dwordx4 v[216:217], off
	v_lshl_add_u64 v[216:217], s[62:63], 0, v[144:145]
	s_add_i32 m0, s61, 0x2000
	s_nop 0
	global_load_lds_dwordx4 v[216:217], off
	v_lshl_add_u64 v[216:217], s[40:41], 0, v[150:151]
	s_mov_b32 m0, s37
	s_nop 0
	global_load_lds_dwordx4 v[216:217], off
	s_mov_b32 m0, s46
	s_nop 0
	global_load_lds_dwordx4 v[218:219], off
	s_waitcnt vmcnt(8)
	s_waitcnt lgkmcnt(0)
	s_setprio 1
	s_barrier
	v_mfma_f32_16x16x32_bf16 v[60:63], v[120:123], v[182:185], v[60:63]
	v_mfma_f32_16x16x32_bf16 v[56:59], v[128:131], v[182:185], v[56:59]
	v_mfma_f32_16x16x32_bf16 v[44:47], v[120:123], v[190:193], v[44:47]
	v_mfma_f32_16x16x32_bf16 v[40:43], v[128:131], v[190:193], v[40:43]
	v_mfma_f32_16x16x32_bf16 v[28:31], v[120:123], v[198:201], v[28:31]
	v_mfma_f32_16x16x32_bf16 v[24:27], v[128:131], v[198:201], v[24:27]
	v_mfma_f32_16x16x32_bf16 v[12:15], v[120:123], v[206:209], v[12:15]
	v_mfma_f32_16x16x32_bf16 v[8:11], v[128:131], v[206:209], v[8:11]
	v_mfma_f32_16x16x32_bf16 v[60:63], v[124:127], v[186:189], v[60:63]
	v_mfma_f32_16x16x32_bf16 v[56:59], v[132:135], v[186:189], v[56:59]
	v_mfma_f32_16x16x32_bf16 v[44:47], v[124:127], v[194:197], v[44:47]
	v_mfma_f32_16x16x32_bf16 v[40:43], v[132:135], v[194:197], v[40:43]
	v_mfma_f32_16x16x32_bf16 v[28:31], v[124:127], v[202:205], v[28:31]
	v_mfma_f32_16x16x32_bf16 v[24:27], v[132:135], v[202:205], v[24:27]
	v_mfma_f32_16x16x32_bf16 v[12:15], v[124:127], v[210:213], v[12:15]
	v_mfma_f32_16x16x32_bf16 v[8:11], v[132:135], v[210:213], v[8:11]
	v_mfma_f32_16x16x32_bf16 v[52:55], v[160:163], v[182:185], v[52:55]
	v_mfma_f32_16x16x32_bf16 v[48:51], v[174:177], v[182:185], v[48:51]
	v_mfma_f32_16x16x32_bf16 v[36:39], v[160:163], v[190:193], v[36:39]
	v_mfma_f32_16x16x32_bf16 v[32:35], v[174:177], v[190:193], v[32:35]
	v_mfma_f32_16x16x32_bf16 v[20:23], v[160:163], v[198:201], v[20:23]
	v_mfma_f32_16x16x32_bf16 v[16:19], v[174:177], v[198:201], v[16:19]
	v_mfma_f32_16x16x32_bf16 v[4:7], v[160:163], v[206:209], v[4:7]
	v_mfma_f32_16x16x32_bf16 v[0:3], v[174:177], v[206:209], v[0:3]
	v_mfma_f32_16x16x32_bf16 v[52:55], v[170:173], v[186:189], v[52:55]
	v_mfma_f32_16x16x32_bf16 v[48:51], v[178:181], v[186:189], v[48:51]
	v_mfma_f32_16x16x32_bf16 v[36:39], v[170:173], v[194:197], v[36:39]
	v_mfma_f32_16x16x32_bf16 v[32:35], v[178:181], v[194:197], v[32:35]
	v_mfma_f32_16x16x32_bf16 v[20:23], v[170:173], v[202:205], v[20:23]
	v_mfma_f32_16x16x32_bf16 v[16:19], v[178:181], v[202:205], v[16:19]
	v_mfma_f32_16x16x32_bf16 v[4:7], v[170:173], v[210:213], v[4:7]
	v_mfma_f32_16x16x32_bf16 v[0:3], v[178:181], v[210:213], v[0:3]
	s_barrier
	s_setprio 0
	s_add_i32 s61, 0, 0x18000
	s_add_i32 s62, 0, 0x1c000
	v_add_u32_e32 v132, s61, v166
	v_add_u32_e32 v178, s62, v166
	ds_read_b128 v[120:123], v132
	ds_read_b128 v[124:127], v132 offset:1024
	ds_read_b128 v[128:131], v132 offset:2048
	ds_read_b128 v[132:135], v132 offset:3072
	ds_read_b128 v[160:163], v178
	ds_read_b128 v[170:173], v178 offset:1024
	ds_read_b128 v[174:177], v178 offset:2048
	ds_read_b128 v[178:181], v178 offset:3072
	s_add_u32 s40, s40, 0x80000
	s_addc_u32 s41, s41, 0
	s_mov_b32 m0, s47
	v_lshl_add_u64 v[220:221], s[40:41], 0, v[150:151]
	ds_read_b128 v[182:185], v169 offset:32768
	ds_read_b128 v[186:189], v169 offset:33792
	ds_read_b128 v[190:193], v169 offset:34816
	ds_read_b128 v[194:197], v169 offset:35840
	ds_read_b128 v[198:201], v169 offset:36864
	ds_read_b128 v[202:205], v169 offset:37888
	ds_read_b128 v[206:209], v169 offset:38912
	ds_read_b128 v[210:213], v169 offset:39936
	global_load_lds_dwordx4 v[220:221], off
	v_lshl_add_u64 v[220:221], s[40:41], 0, v[146:147]
	s_mov_b32 m0, s48
	s_nop 0
	global_load_lds_dwordx4 v[220:221], off
	s_waitcnt vmcnt(8)
	s_waitcnt lgkmcnt(0)
	s_setprio 1
	s_barrier
	v_mfma_f32_16x16x32_bf16 v[140:143], v[120:123], v[182:185], v[140:143]
	v_mfma_f32_16x16x32_bf16 v[136:139], v[128:131], v[182:185], v[136:139]
	v_mfma_f32_16x16x32_bf16 v[108:111], v[120:123], v[190:193], v[108:111]
	v_mfma_f32_16x16x32_bf16 v[104:107], v[128:131], v[190:193], v[104:107]
	v_mfma_f32_16x16x32_bf16 v[92:95], v[120:123], v[198:201], v[92:95]
	v_mfma_f32_16x16x32_bf16 v[88:91], v[128:131], v[198:201], v[88:91]
	v_mfma_f32_16x16x32_bf16 v[76:79], v[120:123], v[206:209], v[76:79]
	v_mfma_f32_16x16x32_bf16 v[72:75], v[128:131], v[206:209], v[72:75]
	v_mfma_f32_16x16x32_bf16 v[140:143], v[124:127], v[186:189], v[140:143]
	v_mfma_f32_16x16x32_bf16 v[136:139], v[132:135], v[186:189], v[136:139]
	v_mfma_f32_16x16x32_bf16 v[108:111], v[124:127], v[194:197], v[108:111]
	v_mfma_f32_16x16x32_bf16 v[104:107], v[132:135], v[194:197], v[104:107]
	v_mfma_f32_16x16x32_bf16 v[92:95], v[124:127], v[202:205], v[92:95]
	v_mfma_f32_16x16x32_bf16 v[88:91], v[132:135], v[202:205], v[88:91]
	v_mfma_f32_16x16x32_bf16 v[76:79], v[124:127], v[210:213], v[76:79]
	v_mfma_f32_16x16x32_bf16 v[72:75], v[132:135], v[210:213], v[72:75]
	v_mfma_f32_16x16x32_bf16 v[116:119], v[160:163], v[182:185], v[116:119]
	v_mfma_f32_16x16x32_bf16 v[112:115], v[174:177], v[182:185], v[112:115]
	v_mfma_f32_16x16x32_bf16 v[100:103], v[160:163], v[190:193], v[100:103]
	v_mfma_f32_16x16x32_bf16 v[96:99], v[174:177], v[190:193], v[96:99]
	v_mfma_f32_16x16x32_bf16 v[84:87], v[160:163], v[198:201], v[84:87]
	v_mfma_f32_16x16x32_bf16 v[80:83], v[174:177], v[198:201], v[80:83]
	v_mfma_f32_16x16x32_bf16 v[68:71], v[160:163], v[206:209], v[68:71]
	v_mfma_f32_16x16x32_bf16 v[64:67], v[174:177], v[206:209], v[64:67]
	v_mfma_f32_16x16x32_bf16 v[116:119], v[170:173], v[186:189], v[116:119]
	v_mfma_f32_16x16x32_bf16 v[112:115], v[178:181], v[186:189], v[112:115]
	v_mfma_f32_16x16x32_bf16 v[100:103], v[170:173], v[194:197], v[100:103]
	v_mfma_f32_16x16x32_bf16 v[96:99], v[178:181], v[194:197], v[96:99]
	v_mfma_f32_16x16x32_bf16 v[84:87], v[170:173], v[202:205], v[84:87]
	v_mfma_f32_16x16x32_bf16 v[80:83], v[178:181], v[202:205], v[80:83]
	v_mfma_f32_16x16x32_bf16 v[68:71], v[170:173], v[210:213], v[68:71]
	v_mfma_f32_16x16x32_bf16 v[64:67], v[178:181], v[210:213], v[64:67]
	s_barrier
	s_setprio 0
	s_add_i32 s40, s61, s44
	v_lshl_add_u64 v[164:165], v[164:165], 0, s[14:15]
	s_mov_b32 m0, s40
	ds_read_b128 v[182:185], v169 offset:49152
	ds_read_b128 v[186:189], v169 offset:50176
	ds_read_b128 v[190:193], v169 offset:51200
	ds_read_b128 v[194:197], v169 offset:52224
	ds_read_b128 v[198:201], v169 offset:53248
	ds_read_b128 v[202:205], v169 offset:54272
	ds_read_b128 v[206:209], v169 offset:55296
	ds_read_b128 v[210:213], v169 offset:56320
	global_load_lds_dwordx4 v[164:165], off
	s_add_i32 m0, s40, 0x2000
	s_add_u32 s38, s38, 0x20080
	v_lshl_add_u64 v[164:165], v[214:215], 0, s[14:15]
	s_addc_u32 s39, s39, 0
	s_add_i32 s40, s62, s44
	global_load_lds_dwordx4 v[164:165], off
	v_lshl_add_u64 v[164:165], s[38:39], 0, v[148:149]
	s_mov_b32 m0, s40
	s_nop 0
	global_load_lds_dwordx4 v[164:165], off
	v_lshl_add_u64 v[164:165], s[38:39], 0, v[144:145]
	s_add_i32 m0, s40, 0x2000
	s_nop 0
	global_load_lds_dwordx4 v[164:165], off
	v_lshl_add_u64 v[164:165], v[216:217], 0, s[14:15]
	s_mov_b32 m0, s52
	s_nop 0
	global_load_lds_dwordx4 v[164:165], off
	v_lshl_add_u64 v[164:165], v[218:219], 0, s[14:15]
	s_mov_b32 m0, s53
	s_nop 0
	global_load_lds_dwordx4 v[164:165], off
	s_waitcnt vmcnt(8)
	s_waitcnt lgkmcnt(0)
	s_setprio 1
	s_barrier
	v_mfma_f32_16x16x32_bf16 v[60:63], v[120:123], v[182:185], v[60:63]
	v_mfma_f32_16x16x32_bf16 v[56:59], v[128:131], v[182:185], v[56:59]
	v_mfma_f32_16x16x32_bf16 v[44:47], v[120:123], v[190:193], v[44:47]
	v_mfma_f32_16x16x32_bf16 v[40:43], v[128:131], v[190:193], v[40:43]
	v_mfma_f32_16x16x32_bf16 v[28:31], v[120:123], v[198:201], v[28:31]
	v_mfma_f32_16x16x32_bf16 v[24:27], v[128:131], v[198:201], v[24:27]
	v_mfma_f32_16x16x32_bf16 v[12:15], v[120:123], v[206:209], v[12:15]
	v_mfma_f32_16x16x32_bf16 v[8:11], v[128:131], v[206:209], v[8:11]
	v_mfma_f32_16x16x32_bf16 v[60:63], v[124:127], v[186:189], v[60:63]
	v_mfma_f32_16x16x32_bf16 v[56:59], v[132:135], v[186:189], v[56:59]
	v_mfma_f32_16x16x32_bf16 v[44:47], v[124:127], v[194:197], v[44:47]
	v_mfma_f32_16x16x32_bf16 v[40:43], v[132:135], v[194:197], v[40:43]
	v_mfma_f32_16x16x32_bf16 v[28:31], v[124:127], v[202:205], v[28:31]
	v_mfma_f32_16x16x32_bf16 v[24:27], v[132:135], v[202:205], v[24:27]
	v_mfma_f32_16x16x32_bf16 v[12:15], v[124:127], v[210:213], v[12:15]
	v_mfma_f32_16x16x32_bf16 v[8:11], v[132:135], v[210:213], v[8:11]
	v_mfma_f32_16x16x32_bf16 v[52:55], v[160:163], v[182:185], v[52:55]
	v_mfma_f32_16x16x32_bf16 v[48:51], v[174:177], v[182:185], v[48:51]
	v_mfma_f32_16x16x32_bf16 v[36:39], v[160:163], v[190:193], v[36:39]
	v_mfma_f32_16x16x32_bf16 v[32:35], v[174:177], v[190:193], v[32:35]
	v_mfma_f32_16x16x32_bf16 v[20:23], v[160:163], v[198:201], v[20:23]
	v_mfma_f32_16x16x32_bf16 v[16:19], v[174:177], v[198:201], v[16:19]
	v_mfma_f32_16x16x32_bf16 v[4:7], v[160:163], v[206:209], v[4:7]
	v_mfma_f32_16x16x32_bf16 v[0:3], v[174:177], v[206:209], v[0:3]
	v_mfma_f32_16x16x32_bf16 v[52:55], v[170:173], v[186:189], v[52:55]
	v_mfma_f32_16x16x32_bf16 v[48:51], v[178:181], v[186:189], v[48:51]
	v_mfma_f32_16x16x32_bf16 v[36:39], v[170:173], v[194:197], v[36:39]
	v_mfma_f32_16x16x32_bf16 v[32:35], v[178:181], v[194:197], v[32:35]
	v_mfma_f32_16x16x32_bf16 v[20:23], v[170:173], v[202:205], v[20:23]
	v_mfma_f32_16x16x32_bf16 v[16:19], v[178:181], v[202:205], v[16:19]
	v_mfma_f32_16x16x32_bf16 v[4:7], v[170:173], v[210:213], v[4:7]
	v_mfma_f32_16x16x32_bf16 v[0:3], v[178:181], v[210:213], v[0:3]
	s_barrier
	s_setprio 0
	s_add_i32 s60, s60, 2
	s_add_u32 s2, s2, 0x100
	s_addc_u32 s3, s3, 0
	s_add_u32 s29, s29, 0x100
	s_addc_u32 s59, s59, 0
	s_cmp_gt_u32 s60, 5
	s_cbranch_scc0 .LBB0_341
	s_and_b64 vcc, exec, s[12:13]
	s_cbranch_vccz .LBB0_344
	s_barrier

.LBB0_493:
	s_add_u32 s24, s24, 0x40080
	s_addc_u32 s25, s25, 0
	s_add_u32 s15, s26, 0x100
	s_addc_u32 s17, s27, 0
	s_mov_b32 s50, -2
	ds_read_b128 v[76:79], v165
	ds_read_b128 v[80:83], v165 offset:1024
	ds_read_b128 v[84:87], v165 offset:2048
	ds_read_b128 v[88:91], v165 offset:3072
	ds_read_b128 v[160:163], v166
	ds_read_b128 v[168:171], v166 offset:1024
	ds_read_b128 v[172:175], v166 offset:2048
	ds_read_b128 v[176:179], v166 offset:3072
	s_add_u32 s26, s24, 0xfffc0080
	s_addc_u32 s27, s25, -1
	s_cmp_eq_u32 s50, 12
	s_cselect_b32 s29, s19, s27
	s_cselect_b32 s28, s18, s26
	s_cselect_b32 s27, s21, s17
	s_cselect_b32 s26, s20, s15
	v_lshl_add_u64 v[212:213], s[24:25], 0, v[152:153]
	s_add_i32 m0, s23, 0xc000
	ds_read_b128 v[180:183], v167
	ds_read_b128 v[184:187], v167 offset:1024
	ds_read_b128 v[188:191], v167 offset:2048
	ds_read_b128 v[192:195], v167 offset:3072
	ds_read_b128 v[196:199], v167 offset:4096
	ds_read_b128 v[200:203], v167 offset:5120
	ds_read_b128 v[204:207], v167 offset:6144
	ds_read_b128 v[208:211], v167 offset:7168
	global_load_lds_dwordx4 v[212:213], off
	v_lshl_add_u64 v[212:213], s[24:25], 0, v[154:155]
	s_add_i32 m0, s23, 0xe000
	s_nop 0
	global_load_lds_dwordx4 v[212:213], off
	s_waitcnt vmcnt(8)
	s_waitcnt lgkmcnt(0)
	s_setprio 1
	s_barrier
	v_mfma_i32_16x16x64_i8 v[140:143], v[76:79], v[180:183], 0
	v_mfma_i32_16x16x64_i8 v[136:139], v[84:87], v[180:183], 0
	v_mfma_i32_16x16x64_i8 v[124:127], v[76:79], v[188:191], 0
	v_mfma_i32_16x16x64_i8 v[120:123], v[84:87], v[188:191], 0
	v_mfma_i32_16x16x64_i8 v[108:111], v[76:79], v[196:199], 0
	v_mfma_i32_16x16x64_i8 v[104:107], v[84:87], v[196:199], 0
	v_mfma_i32_16x16x64_i8 v[92:95], v[76:79], v[204:207], 0
	v_mfma_i32_16x16x64_i8 v[72:75], v[84:87], v[204:207], 0
	v_mfma_i32_16x16x64_i8 v[140:143], v[80:83], v[184:187], v[140:143]
	v_mfma_i32_16x16x64_i8 v[136:139], v[88:91], v[184:187], v[136:139]
	v_mfma_i32_16x16x64_i8 v[124:127], v[80:83], v[192:195], v[124:127]
	v_mfma_i32_16x16x64_i8 v[120:123], v[88:91], v[192:195], v[120:123]
	v_mfma_i32_16x16x64_i8 v[108:111], v[80:83], v[200:203], v[108:111]
	v_mfma_i32_16x16x64_i8 v[104:107], v[88:91], v[200:203], v[104:107]
	v_mfma_i32_16x16x64_i8 v[92:95], v[80:83], v[208:211], v[92:95]
	v_mfma_i32_16x16x64_i8 v[72:75], v[88:91], v[208:211], v[72:75]
	v_mfma_i32_16x16x64_i8 v[132:135], v[160:163], v[180:183], 0
	v_mfma_i32_16x16x64_i8 v[128:131], v[172:175], v[180:183], 0
	v_mfma_i32_16x16x64_i8 v[116:119], v[160:163], v[188:191], 0
	v_mfma_i32_16x16x64_i8 v[112:115], v[172:175], v[188:191], 0
	v_mfma_i32_16x16x64_i8 v[100:103], v[160:163], v[196:199], 0
	v_mfma_i32_16x16x64_i8 v[96:99], v[172:175], v[196:199], 0
	v_mfma_i32_16x16x64_i8 v[68:71], v[160:163], v[204:207], 0
	v_mfma_i32_16x16x64_i8 v[64:67], v[172:175], v[204:207], 0
	v_mfma_i32_16x16x64_i8 v[132:135], v[168:171], v[184:187], v[132:135]
	v_mfma_i32_16x16x64_i8 v[128:131], v[176:179], v[184:187], v[128:131]
	v_mfma_i32_16x16x64_i8 v[116:119], v[168:171], v[192:195], v[116:119]
	v_mfma_i32_16x16x64_i8 v[112:115], v[176:179], v[192:195], v[112:115]
	v_mfma_i32_16x16x64_i8 v[100:103], v[168:171], v[200:203], v[100:103]
	v_mfma_i32_16x16x64_i8 v[96:99], v[176:179], v[200:203], v[96:99]
	v_mfma_i32_16x16x64_i8 v[68:71], v[168:171], v[208:211], v[68:71]
	v_mfma_i32_16x16x64_i8 v[64:67], v[176:179], v[208:211], v[64:67]
	s_barrier
	s_setprio 0
	s_add_i32 s51, s46, s31
	v_lshl_add_u64 v[212:213], s[26:27], 0, v[148:149]
	s_mov_b32 m0, s51
	ds_read_b128 v[180:183], v167 offset:16384
	ds_read_b128 v[184:187], v167 offset:17408
	ds_read_b128 v[188:191], v167 offset:18432
	ds_read_b128 v[192:195], v167 offset:19456
	ds_read_b128 v[196:199], v167 offset:20480
	ds_read_b128 v[200:203], v167 offset:21504
	ds_read_b128 v[204:207], v167 offset:22528
	ds_read_b128 v[208:211], v167 offset:23552
	global_load_lds_dwordx4 v[212:213], off
	s_add_i32 m0, s51, 0x2000
	s_add_u32 s52, s26, 0x40000
	v_lshl_add_u64 v[214:215], s[26:27], 0, v[144:145]
	s_addc_u32 s53, s27, 0
	s_add_i32 s51, s47, s31
	global_load_lds_dwordx4 v[214:215], off
	v_lshl_add_u64 v[216:217], s[52:53], 0, v[148:149]
	s_mov_b32 m0, s51
	v_lshl_add_u64 v[218:219], s[28:29], 0, v[146:147]
	global_load_lds_dwordx4 v[216:217], off
	v_lshl_add_u64 v[216:217], s[52:53], 0, v[144:145]
	s_add_i32 m0, s51, 0x2000
	s_nop 0
	global_load_lds_dwordx4 v[216:217], off
	v_lshl_add_u64 v[216:217], s[28:29], 0, v[150:151]
	s_mov_b32 m0, s23
	s_nop 0
	global_load_lds_dwordx4 v[216:217], off
	s_mov_b32 m0, s35
	s_nop 0
	global_load_lds_dwordx4 v[218:219], off
	s_waitcnt vmcnt(8)
	s_waitcnt lgkmcnt(0)
	s_setprio 1
	s_barrier
	v_mfma_i32_16x16x64_i8 v[60:63], v[76:79], v[180:183], 0
	v_mfma_i32_16x16x64_i8 v[56:59], v[84:87], v[180:183], 0
	v_mfma_i32_16x16x64_i8 v[44:47], v[76:79], v[188:191], 0
	v_mfma_i32_16x16x64_i8 v[40:43], v[84:87], v[188:191], 0
	v_mfma_i32_16x16x64_i8 v[28:31], v[76:79], v[196:199], 0
	v_mfma_i32_16x16x64_i8 v[24:27], v[84:87], v[196:199], 0
	v_mfma_i32_16x16x64_i8 v[12:15], v[76:79], v[204:207], 0
	v_mfma_i32_16x16x64_i8 v[8:11], v[84:87], v[204:207], 0
	v_mfma_i32_16x16x64_i8 v[60:63], v[80:83], v[184:187], v[60:63]
	v_mfma_i32_16x16x64_i8 v[56:59], v[88:91], v[184:187], v[56:59]
	v_mfma_i32_16x16x64_i8 v[44:47], v[80:83], v[192:195], v[44:47]
	v_mfma_i32_16x16x64_i8 v[40:43], v[88:91], v[192:195], v[40:43]
	v_mfma_i32_16x16x64_i8 v[28:31], v[80:83], v[200:203], v[28:31]
	v_mfma_i32_16x16x64_i8 v[24:27], v[88:91], v[200:203], v[24:27]
	v_mfma_i32_16x16x64_i8 v[12:15], v[80:83], v[208:211], v[12:15]
	v_mfma_i32_16x16x64_i8 v[8:11], v[88:91], v[208:211], v[8:11]
	v_mfma_i32_16x16x64_i8 v[52:55], v[160:163], v[180:183], 0
	v_mfma_i32_16x16x64_i8 v[48:51], v[172:175], v[180:183], 0
	v_mfma_i32_16x16x64_i8 v[36:39], v[160:163], v[188:191], 0
	v_mfma_i32_16x16x64_i8 v[32:35], v[172:175], v[188:191], 0
	v_mfma_i32_16x16x64_i8 v[20:23], v[160:163], v[196:199], 0
	v_mfma_i32_16x16x64_i8 v[16:19], v[172:175], v[196:199], 0
	v_mfma_i32_16x16x64_i8 v[4:7], v[160:163], v[204:207], 0
	v_mfma_i32_16x16x64_i8 v[0:3], v[172:175], v[204:207], 0
	v_mfma_i32_16x16x64_i8 v[52:55], v[168:171], v[184:187], v[52:55]
	v_mfma_i32_16x16x64_i8 v[48:51], v[176:179], v[184:187], v[48:51]
	v_mfma_i32_16x16x64_i8 v[36:39], v[168:171], v[192:195], v[36:39]
	v_mfma_i32_16x16x64_i8 v[32:35], v[176:179], v[192:195], v[32:35]
	v_mfma_i32_16x16x64_i8 v[20:23], v[168:171], v[200:203], v[20:23]
	v_mfma_i32_16x16x64_i8 v[16:19], v[176:179], v[200:203], v[16:19]
	v_mfma_i32_16x16x64_i8 v[4:7], v[168:171], v[208:211], v[4:7]
	v_mfma_i32_16x16x64_i8 v[0:3], v[176:179], v[208:211], v[0:3]
	s_barrier
	s_setprio 0
	s_add_i32 s51, 0, 0x18000
	s_add_i32 s52, 0, 0x1c000
	v_add_u32_e32 v88, s51, v164
	v_add_u32_e32 v176, s52, v164
	ds_read_b128 v[76:79], v88
	ds_read_b128 v[80:83], v88 offset:1024
	ds_read_b128 v[84:87], v88 offset:2048
	ds_read_b128 v[88:91], v88 offset:3072
	ds_read_b128 v[160:163], v176
	ds_read_b128 v[168:171], v176 offset:1024
	ds_read_b128 v[172:175], v176 offset:2048
	ds_read_b128 v[176:179], v176 offset:3072
	s_add_u32 s28, s28, 0x40000
	s_addc_u32 s29, s29, 0
	s_mov_b32 m0, s36
	v_lshl_add_u64 v[220:221], s[28:29], 0, v[150:151]
	ds_read_b128 v[180:183], v167 offset:32768
	ds_read_b128 v[184:187], v167 offset:33792
	ds_read_b128 v[188:191], v167 offset:34816
	ds_read_b128 v[192:195], v167 offset:35840
	ds_read_b128 v[196:199], v167 offset:36864
	ds_read_b128 v[200:203], v167 offset:37888
	ds_read_b128 v[204:207], v167 offset:38912
	ds_read_b128 v[208:211], v167 offset:39936
	global_load_lds_dwordx4 v[220:221], off
	v_lshl_add_u64 v[220:221], s[28:29], 0, v[146:147]
	s_mov_b32 m0, s37
	s_nop 0
	global_load_lds_dwordx4 v[220:221], off
	s_waitcnt vmcnt(8)
	s_waitcnt lgkmcnt(0)
	s_setprio 1
	s_barrier
	v_mfma_i32_16x16x64_i8 v[140:143], v[76:79], v[180:183], v[140:143]
	v_mfma_i32_16x16x64_i8 v[136:139], v[84:87], v[180:183], v[136:139]
	v_mfma_i32_16x16x64_i8 v[124:127], v[76:79], v[188:191], v[124:127]
	v_mfma_i32_16x16x64_i8 v[120:123], v[84:87], v[188:191], v[120:123]
	v_mfma_i32_16x16x64_i8 v[108:111], v[76:79], v[196:199], v[108:111]
	v_mfma_i32_16x16x64_i8 v[104:107], v[84:87], v[196:199], v[104:107]
	v_mfma_i32_16x16x64_i8 v[92:95], v[76:79], v[204:207], v[92:95]
	v_mfma_i32_16x16x64_i8 v[72:75], v[84:87], v[204:207], v[72:75]
	v_mfma_i32_16x16x64_i8 v[140:143], v[80:83], v[184:187], v[140:143]
	v_mfma_i32_16x16x64_i8 v[136:139], v[88:91], v[184:187], v[136:139]
	v_mfma_i32_16x16x64_i8 v[124:127], v[80:83], v[192:195], v[124:127]
	v_mfma_i32_16x16x64_i8 v[120:123], v[88:91], v[192:195], v[120:123]
	v_mfma_i32_16x16x64_i8 v[108:111], v[80:83], v[200:203], v[108:111]
	v_mfma_i32_16x16x64_i8 v[104:107], v[88:91], v[200:203], v[104:107]
	v_mfma_i32_16x16x64_i8 v[92:95], v[80:83], v[208:211], v[92:95]
	v_mfma_i32_16x16x64_i8 v[72:75], v[88:91], v[208:211], v[72:75]
	v_mfma_i32_16x16x64_i8 v[132:135], v[160:163], v[180:183], v[132:135]
	v_mfma_i32_16x16x64_i8 v[128:131], v[172:175], v[180:183], v[128:131]
	v_mfma_i32_16x16x64_i8 v[116:119], v[160:163], v[188:191], v[116:119]
	v_mfma_i32_16x16x64_i8 v[112:115], v[172:175], v[188:191], v[112:115]
	v_mfma_i32_16x16x64_i8 v[100:103], v[160:163], v[196:199], v[100:103]
	v_mfma_i32_16x16x64_i8 v[96:99], v[172:175], v[196:199], v[96:99]
	v_mfma_i32_16x16x64_i8 v[68:71], v[160:163], v[204:207], v[68:71]
	v_mfma_i32_16x16x64_i8 v[64:67], v[172:175], v[204:207], v[64:67]
	v_mfma_i32_16x16x64_i8 v[132:135], v[168:171], v[184:187], v[132:135]
	v_mfma_i32_16x16x64_i8 v[128:131], v[176:179], v[184:187], v[128:131]
	v_mfma_i32_16x16x64_i8 v[116:119], v[168:171], v[192:195], v[116:119]
	v_mfma_i32_16x16x64_i8 v[112:115], v[176:179], v[192:195], v[112:115]
	v_mfma_i32_16x16x64_i8 v[100:103], v[168:171], v[200:203], v[100:103]
	v_mfma_i32_16x16x64_i8 v[96:99], v[176:179], v[200:203], v[96:99]
	v_mfma_i32_16x16x64_i8 v[68:71], v[168:171], v[208:211], v[68:71]
	v_mfma_i32_16x16x64_i8 v[64:67], v[176:179], v[208:211], v[64:67]
	s_barrier
	s_setprio 0
	s_add_i32 s28, s51, s31
	v_lshl_add_u64 v[212:213], v[212:213], 0, s[10:11]
	s_mov_b32 m0, s28
	ds_read_b128 v[180:183], v167 offset:49152
	ds_read_b128 v[184:187], v167 offset:50176
	ds_read_b128 v[188:191], v167 offset:51200
	ds_read_b128 v[192:195], v167 offset:52224
	ds_read_b128 v[196:199], v167 offset:53248
	ds_read_b128 v[200:203], v167 offset:54272
	ds_read_b128 v[204:207], v167 offset:55296
	ds_read_b128 v[208:211], v167 offset:56320
	global_load_lds_dwordx4 v[212:213], off
	s_add_i32 m0, s28, 0x2000
	s_add_u32 s26, s26, 0x40080
	v_lshl_add_u64 v[212:213], v[214:215], 0, s[10:11]
	s_addc_u32 s27, s27, 0
	s_add_i32 s28, s52, s31
	global_load_lds_dwordx4 v[212:213], off
	v_lshl_add_u64 v[212:213], s[26:27], 0, v[148:149]
	s_mov_b32 m0, s28
	s_nop 0
	global_load_lds_dwordx4 v[212:213], off
	v_lshl_add_u64 v[212:213], s[26:27], 0, v[144:145]
	s_add_i32 m0, s28, 0x2000
	s_nop 0
	global_load_lds_dwordx4 v[212:213], off
	v_lshl_add_u64 v[212:213], v[216:217], 0, s[10:11]
	s_mov_b32 m0, s44
	s_nop 0
	global_load_lds_dwordx4 v[212:213], off
	v_lshl_add_u64 v[212:213], v[218:219], 0, s[10:11]
	s_mov_b32 m0, s45
	s_nop 0
	global_load_lds_dwordx4 v[212:213], off
	s_waitcnt vmcnt(8)
	s_waitcnt lgkmcnt(0)
	s_setprio 1
	s_barrier
	v_mfma_i32_16x16x64_i8 v[60:63], v[76:79], v[180:183], v[60:63]
	v_mfma_i32_16x16x64_i8 v[56:59], v[84:87], v[180:183], v[56:59]
	v_mfma_i32_16x16x64_i8 v[44:47], v[76:79], v[188:191], v[44:47]
	v_mfma_i32_16x16x64_i8 v[40:43], v[84:87], v[188:191], v[40:43]
	v_mfma_i32_16x16x64_i8 v[28:31], v[76:79], v[196:199], v[28:31]
	v_mfma_i32_16x16x64_i8 v[24:27], v[84:87], v[196:199], v[24:27]
	v_mfma_i32_16x16x64_i8 v[12:15], v[76:79], v[204:207], v[12:15]
	v_mfma_i32_16x16x64_i8 v[8:11], v[84:87], v[204:207], v[8:11]
	v_mfma_i32_16x16x64_i8 v[60:63], v[80:83], v[184:187], v[60:63]
	v_mfma_i32_16x16x64_i8 v[56:59], v[88:91], v[184:187], v[56:59]
	v_mfma_i32_16x16x64_i8 v[44:47], v[80:83], v[192:195], v[44:47]
	v_mfma_i32_16x16x64_i8 v[40:43], v[88:91], v[192:195], v[40:43]
	v_mfma_i32_16x16x64_i8 v[28:31], v[80:83], v[200:203], v[28:31]
	v_mfma_i32_16x16x64_i8 v[24:27], v[88:91], v[200:203], v[24:27]
	v_mfma_i32_16x16x64_i8 v[12:15], v[80:83], v[208:211], v[12:15]
	v_mfma_i32_16x16x64_i8 v[8:11], v[88:91], v[208:211], v[8:11]
	v_mfma_i32_16x16x64_i8 v[52:55], v[160:163], v[180:183], v[52:55]
	v_mfma_i32_16x16x64_i8 v[48:51], v[172:175], v[180:183], v[48:51]
	v_mfma_i32_16x16x64_i8 v[36:39], v[160:163], v[188:191], v[36:39]
	v_mfma_i32_16x16x64_i8 v[32:35], v[172:175], v[188:191], v[32:35]
	v_mfma_i32_16x16x64_i8 v[20:23], v[160:163], v[196:199], v[20:23]
	v_mfma_i32_16x16x64_i8 v[16:19], v[172:175], v[196:199], v[16:19]
	v_mfma_i32_16x16x64_i8 v[4:7], v[160:163], v[204:207], v[4:7]
	v_mfma_i32_16x16x64_i8 v[0:3], v[172:175], v[204:207], v[0:3]
	v_mfma_i32_16x16x64_i8 v[52:55], v[168:171], v[184:187], v[52:55]
	v_mfma_i32_16x16x64_i8 v[48:51], v[176:179], v[184:187], v[48:51]
	v_mfma_i32_16x16x64_i8 v[36:39], v[168:171], v[192:195], v[36:39]
	v_mfma_i32_16x16x64_i8 v[32:35], v[176:179], v[192:195], v[32:35]
	v_mfma_i32_16x16x64_i8 v[20:23], v[168:171], v[200:203], v[20:23]
	v_mfma_i32_16x16x64_i8 v[16:19], v[176:179], v[200:203], v[16:19]
	v_mfma_i32_16x16x64_i8 v[4:7], v[168:171], v[208:211], v[4:7]
	v_mfma_i32_16x16x64_i8 v[0:3], v[176:179], v[208:211], v[0:3]
	s_barrier
	s_setprio 0
	s_add_i32 s50, s50, 2
	s_add_u32 s24, s24, 0x100
	s_addc_u32 s25, s25, 0
	s_add_u32 s15, s15, 0x100
	s_addc_u32 s17, s17, 0
.LBB0_494:
	ds_read_b128 v[76:79], v165
	ds_read_b128 v[80:83], v165 offset:1024
	ds_read_b128 v[84:87], v165 offset:2048
	ds_read_b128 v[88:91], v165 offset:3072
	ds_read_b128 v[160:163], v166
	ds_read_b128 v[168:171], v166 offset:1024
	ds_read_b128 v[172:175], v166 offset:2048
	ds_read_b128 v[176:179], v166 offset:3072
	s_add_u32 s26, s24, 0xfffc0080
	s_addc_u32 s27, s25, -1
	s_cmp_eq_u32 s50, 12
	s_cselect_b32 s29, s19, s27
	s_cselect_b32 s28, s18, s26
	s_cselect_b32 s27, s21, s17
	s_cselect_b32 s26, s20, s15
	v_lshl_add_u64 v[212:213], s[24:25], 0, v[152:153]
	s_add_i32 m0, s23, 0xc000
	ds_read_b128 v[180:183], v167
	ds_read_b128 v[184:187], v167 offset:1024
	ds_read_b128 v[188:191], v167 offset:2048
	ds_read_b128 v[192:195], v167 offset:3072
	ds_read_b128 v[196:199], v167 offset:4096
	ds_read_b128 v[200:203], v167 offset:5120
	ds_read_b128 v[204:207], v167 offset:6144
	ds_read_b128 v[208:211], v167 offset:7168
	global_load_lds_dwordx4 v[212:213], off
	v_lshl_add_u64 v[212:213], s[24:25], 0, v[154:155]
	s_add_i32 m0, s23, 0xe000
	s_nop 0
	global_load_lds_dwordx4 v[212:213], off
	s_waitcnt vmcnt(8)
	s_waitcnt lgkmcnt(0)
	s_setprio 1
	s_barrier
	v_mfma_i32_16x16x64_i8 v[140:143], v[76:79], v[180:183], v[140:143]
	v_mfma_i32_16x16x64_i8 v[136:139], v[84:87], v[180:183], v[136:139]
	v_mfma_i32_16x16x64_i8 v[124:127], v[76:79], v[188:191], v[124:127]
	v_mfma_i32_16x16x64_i8 v[120:123], v[84:87], v[188:191], v[120:123]
	v_mfma_i32_16x16x64_i8 v[108:111], v[76:79], v[196:199], v[108:111]
	v_mfma_i32_16x16x64_i8 v[104:107], v[84:87], v[196:199], v[104:107]
	v_mfma_i32_16x16x64_i8 v[92:95], v[76:79], v[204:207], v[92:95]
	v_mfma_i32_16x16x64_i8 v[72:75], v[84:87], v[204:207], v[72:75]
	v_mfma_i32_16x16x64_i8 v[140:143], v[80:83], v[184:187], v[140:143]
	v_mfma_i32_16x16x64_i8 v[136:139], v[88:91], v[184:187], v[136:139]
	v_mfma_i32_16x16x64_i8 v[124:127], v[80:83], v[192:195], v[124:127]
	v_mfma_i32_16x16x64_i8 v[120:123], v[88:91], v[192:195], v[120:123]
	v_mfma_i32_16x16x64_i8 v[108:111], v[80:83], v[200:203], v[108:111]
	v_mfma_i32_16x16x64_i8 v[104:107], v[88:91], v[200:203], v[104:107]
	v_mfma_i32_16x16x64_i8 v[92:95], v[80:83], v[208:211], v[92:95]
	v_mfma_i32_16x16x64_i8 v[72:75], v[88:91], v[208:211], v[72:75]
	v_mfma_i32_16x16x64_i8 v[132:135], v[160:163], v[180:183], v[132:135]
	v_mfma_i32_16x16x64_i8 v[128:131], v[172:175], v[180:183], v[128:131]
	v_mfma_i32_16x16x64_i8 v[116:119], v[160:163], v[188:191], v[116:119]
	v_mfma_i32_16x16x64_i8 v[112:115], v[172:175], v[188:191], v[112:115]
	v_mfma_i32_16x16x64_i8 v[100:103], v[160:163], v[196:199], v[100:103]
	v_mfma_i32_16x16x64_i8 v[96:99], v[172:175], v[196:199], v[96:99]
	v_mfma_i32_16x16x64_i8 v[68:71], v[160:163], v[204:207], v[68:71]
	v_mfma_i32_16x16x64_i8 v[64:67], v[172:175], v[204:207], v[64:67]
	v_mfma_i32_16x16x64_i8 v[132:135], v[168:171], v[184:187], v[132:135]
	v_mfma_i32_16x16x64_i8 v[128:131], v[176:179], v[184:187], v[128:131]
	v_mfma_i32_16x16x64_i8 v[116:119], v[168:171], v[192:195], v[116:119]
	v_mfma_i32_16x16x64_i8 v[112:115], v[176:179], v[192:195], v[112:115]
	v_mfma_i32_16x16x64_i8 v[100:103], v[168:171], v[200:203], v[100:103]
	v_mfma_i32_16x16x64_i8 v[96:99], v[176:179], v[200:203], v[96:99]
	v_mfma_i32_16x16x64_i8 v[68:71], v[168:171], v[208:211], v[68:71]
	v_mfma_i32_16x16x64_i8 v[64:67], v[176:179], v[208:211], v[64:67]
	s_barrier
	s_setprio 0
	s_add_i32 s51, s46, s31
	v_lshl_add_u64 v[212:213], s[26:27], 0, v[148:149]
	s_mov_b32 m0, s51
	ds_read_b128 v[180:183], v167 offset:16384
	ds_read_b128 v[184:187], v167 offset:17408
	ds_read_b128 v[188:191], v167 offset:18432
	ds_read_b128 v[192:195], v167 offset:19456
	ds_read_b128 v[196:199], v167 offset:20480
	ds_read_b128 v[200:203], v167 offset:21504
	ds_read_b128 v[204:207], v167 offset:22528
	ds_read_b128 v[208:211], v167 offset:23552
	global_load_lds_dwordx4 v[212:213], off
	s_add_i32 m0, s51, 0x2000
	s_add_u32 s52, s26, 0x40000
	v_lshl_add_u64 v[214:215], s[26:27], 0, v[144:145]
	s_addc_u32 s53, s27, 0
	s_add_i32 s51, s47, s31
	global_load_lds_dwordx4 v[214:215], off
	v_lshl_add_u64 v[216:217], s[52:53], 0, v[148:149]
	s_mov_b32 m0, s51
	v_lshl_add_u64 v[218:219], s[28:29], 0, v[146:147]
	global_load_lds_dwordx4 v[216:217], off
	v_lshl_add_u64 v[216:217], s[52:53], 0, v[144:145]
	s_add_i32 m0, s51, 0x2000
	s_nop 0
	global_load_lds_dwordx4 v[216:217], off
	v_lshl_add_u64 v[216:217], s[28:29], 0, v[150:151]
	s_mov_b32 m0, s23
	s_nop 0
	global_load_lds_dwordx4 v[216:217], off
	s_mov_b32 m0, s35
	s_nop 0
	global_load_lds_dwordx4 v[218:219], off
	s_waitcnt vmcnt(8)
	s_waitcnt lgkmcnt(0)
	s_setprio 1
	s_barrier
	v_mfma_i32_16x16x64_i8 v[60:63], v[76:79], v[180:183], v[60:63]
	v_mfma_i32_16x16x64_i8 v[56:59], v[84:87], v[180:183], v[56:59]
	v_mfma_i32_16x16x64_i8 v[44:47], v[76:79], v[188:191], v[44:47]
	v_mfma_i32_16x16x64_i8 v[40:43], v[84:87], v[188:191], v[40:43]
	v_mfma_i32_16x16x64_i8 v[28:31], v[76:79], v[196:199], v[28:31]
	v_mfma_i32_16x16x64_i8 v[24:27], v[84:87], v[196:199], v[24:27]
	v_mfma_i32_16x16x64_i8 v[12:15], v[76:79], v[204:207], v[12:15]
	v_mfma_i32_16x16x64_i8 v[8:11], v[84:87], v[204:207], v[8:11]
	v_mfma_i32_16x16x64_i8 v[60:63], v[80:83], v[184:187], v[60:63]
	v_mfma_i32_16x16x64_i8 v[56:59], v[88:91], v[184:187], v[56:59]
	v_mfma_i32_16x16x64_i8 v[44:47], v[80:83], v[192:195], v[44:47]
	v_mfma_i32_16x16x64_i8 v[40:43], v[88:91], v[192:195], v[40:43]
	v_mfma_i32_16x16x64_i8 v[28:31], v[80:83], v[200:203], v[28:31]
	v_mfma_i32_16x16x64_i8 v[24:27], v[88:91], v[200:203], v[24:27]
	v_mfma_i32_16x16x64_i8 v[12:15], v[80:83], v[208:211], v[12:15]
	v_mfma_i32_16x16x64_i8 v[8:11], v[88:91], v[208:211], v[8:11]
	v_mfma_i32_16x16x64_i8 v[52:55], v[160:163], v[180:183], v[52:55]
	v_mfma_i32_16x16x64_i8 v[48:51], v[172:175], v[180:183], v[48:51]
	v_mfma_i32_16x16x64_i8 v[36:39], v[160:163], v[188:191], v[36:39]
	v_mfma_i32_16x16x64_i8 v[32:35], v[172:175], v[188:191], v[32:35]
	v_mfma_i32_16x16x64_i8 v[20:23], v[160:163], v[196:199], v[20:23]
	v_mfma_i32_16x16x64_i8 v[16:19], v[172:175], v[196:199], v[16:19]
	v_mfma_i32_16x16x64_i8 v[4:7], v[160:163], v[204:207], v[4:7]
	v_mfma_i32_16x16x64_i8 v[0:3], v[172:175], v[204:207], v[0:3]
	v_mfma_i32_16x16x64_i8 v[52:55], v[168:171], v[184:187], v[52:55]
	v_mfma_i32_16x16x64_i8 v[48:51], v[176:179], v[184:187], v[48:51]
	v_mfma_i32_16x16x64_i8 v[36:39], v[168:171], v[192:195], v[36:39]
	v_mfma_i32_16x16x64_i8 v[32:35], v[176:179], v[192:195], v[32:35]
	v_mfma_i32_16x16x64_i8 v[20:23], v[168:171], v[200:203], v[20:23]
	v_mfma_i32_16x16x64_i8 v[16:19], v[176:179], v[200:203], v[16:19]
	v_mfma_i32_16x16x64_i8 v[4:7], v[168:171], v[208:211], v[4:7]
	v_mfma_i32_16x16x64_i8 v[0:3], v[176:179], v[208:211], v[0:3]
	s_barrier
	s_setprio 0
	s_add_i32 s51, 0, 0x18000
	s_add_i32 s52, 0, 0x1c000
	v_add_u32_e32 v88, s51, v164
	v_add_u32_e32 v176, s52, v164
	ds_read_b128 v[76:79], v88
	ds_read_b128 v[80:83], v88 offset:1024
	ds_read_b128 v[84:87], v88 offset:2048
	ds_read_b128 v[88:91], v88 offset:3072
	ds_read_b128 v[160:163], v176
	ds_read_b128 v[168:171], v176 offset:1024
	ds_read_b128 v[172:175], v176 offset:2048
	ds_read_b128 v[176:179], v176 offset:3072
	s_add_u32 s28, s28, 0x40000
	s_addc_u32 s29, s29, 0
	s_mov_b32 m0, s36
	v_lshl_add_u64 v[220:221], s[28:29], 0, v[150:151]
	ds_read_b128 v[180:183], v167 offset:32768
	ds_read_b128 v[184:187], v167 offset:33792
	ds_read_b128 v[188:191], v167 offset:34816
	ds_read_b128 v[192:195], v167 offset:35840
	ds_read_b128 v[196:199], v167 offset:36864
	ds_read_b128 v[200:203], v167 offset:37888
	ds_read_b128 v[204:207], v167 offset:38912
	ds_read_b128 v[208:211], v167 offset:39936
	global_load_lds_dwordx4 v[220:221], off
	v_lshl_add_u64 v[220:221], s[28:29], 0, v[146:147]
	s_mov_b32 m0, s37
	s_nop 0
	global_load_lds_dwordx4 v[220:221], off
	s_waitcnt vmcnt(8)
	s_waitcnt lgkmcnt(0)
	s_setprio 1
	s_barrier
	v_mfma_i32_16x16x64_i8 v[140:143], v[76:79], v[180:183], v[140:143]
	v_mfma_i32_16x16x64_i8 v[136:139], v[84:87], v[180:183], v[136:139]
	v_mfma_i32_16x16x64_i8 v[124:127], v[76:79], v[188:191], v[124:127]
	v_mfma_i32_16x16x64_i8 v[120:123], v[84:87], v[188:191], v[120:123]
	v_mfma_i32_16x16x64_i8 v[108:111], v[76:79], v[196:199], v[108:111]
	v_mfma_i32_16x16x64_i8 v[104:107], v[84:87], v[196:199], v[104:107]
	v_mfma_i32_16x16x64_i8 v[92:95], v[76:79], v[204:207], v[92:95]
	v_mfma_i32_16x16x64_i8 v[72:75], v[84:87], v[204:207], v[72:75]
	v_mfma_i32_16x16x64_i8 v[140:143], v[80:83], v[184:187], v[140:143]
	v_mfma_i32_16x16x64_i8 v[136:139], v[88:91], v[184:187], v[136:139]
	v_mfma_i32_16x16x64_i8 v[124:127], v[80:83], v[192:195], v[124:127]
	v_mfma_i32_16x16x64_i8 v[120:123], v[88:91], v[192:195], v[120:123]
	v_mfma_i32_16x16x64_i8 v[108:111], v[80:83], v[200:203], v[108:111]
	v_mfma_i32_16x16x64_i8 v[104:107], v[88:91], v[200:203], v[104:107]
	v_mfma_i32_16x16x64_i8 v[92:95], v[80:83], v[208:211], v[92:95]
	v_mfma_i32_16x16x64_i8 v[72:75], v[88:91], v[208:211], v[72:75]
	v_mfma_i32_16x16x64_i8 v[132:135], v[160:163], v[180:183], v[132:135]
	v_mfma_i32_16x16x64_i8 v[128:131], v[172:175], v[180:183], v[128:131]
	v_mfma_i32_16x16x64_i8 v[116:119], v[160:163], v[188:191], v[116:119]
	v_mfma_i32_16x16x64_i8 v[112:115], v[172:175], v[188:191], v[112:115]
	v_mfma_i32_16x16x64_i8 v[100:103], v[160:163], v[196:199], v[100:103]
	v_mfma_i32_16x16x64_i8 v[96:99], v[172:175], v[196:199], v[96:99]
	v_mfma_i32_16x16x64_i8 v[68:71], v[160:163], v[204:207], v[68:71]
	v_mfma_i32_16x16x64_i8 v[64:67], v[172:175], v[204:207], v[64:67]
	v_mfma_i32_16x16x64_i8 v[132:135], v[168:171], v[184:187], v[132:135]
	v_mfma_i32_16x16x64_i8 v[128:131], v[176:179], v[184:187], v[128:131]
	v_mfma_i32_16x16x64_i8 v[116:119], v[168:171], v[192:195], v[116:119]
	v_mfma_i32_16x16x64_i8 v[112:115], v[176:179], v[192:195], v[112:115]
	v_mfma_i32_16x16x64_i8 v[100:103], v[168:171], v[200:203], v[100:103]
	v_mfma_i32_16x16x64_i8 v[96:99], v[176:179], v[200:203], v[96:99]
	v_mfma_i32_16x16x64_i8 v[68:71], v[168:171], v[208:211], v[68:71]
	v_mfma_i32_16x16x64_i8 v[64:67], v[176:179], v[208:211], v[64:67]
	s_barrier
	s_setprio 0
	s_add_i32 s28, s51, s31
	v_lshl_add_u64 v[212:213], v[212:213], 0, s[10:11]
	s_mov_b32 m0, s28
	ds_read_b128 v[180:183], v167 offset:49152
	ds_read_b128 v[184:187], v167 offset:50176
	ds_read_b128 v[188:191], v167 offset:51200
	ds_read_b128 v[192:195], v167 offset:52224
	ds_read_b128 v[196:199], v167 offset:53248
	ds_read_b128 v[200:203], v167 offset:54272
	ds_read_b128 v[204:207], v167 offset:55296
	ds_read_b128 v[208:211], v167 offset:56320
	global_load_lds_dwordx4 v[212:213], off
	s_add_i32 m0, s28, 0x2000
	s_add_u32 s26, s26, 0x40080
	v_lshl_add_u64 v[212:213], v[214:215], 0, s[10:11]
	s_addc_u32 s27, s27, 0
	s_add_i32 s28, s52, s31
	global_load_lds_dwordx4 v[212:213], off
	v_lshl_add_u64 v[212:213], s[26:27], 0, v[148:149]
	s_mov_b32 m0, s28
	s_nop 0
	global_load_lds_dwordx4 v[212:213], off
	v_lshl_add_u64 v[212:213], s[26:27], 0, v[144:145]
	s_add_i32 m0, s28, 0x2000
	s_nop 0
	global_load_lds_dwordx4 v[212:213], off
	v_lshl_add_u64 v[212:213], v[216:217], 0, s[10:11]
	s_mov_b32 m0, s44
	s_nop 0
	global_load_lds_dwordx4 v[212:213], off
	v_lshl_add_u64 v[212:213], v[218:219], 0, s[10:11]
	s_mov_b32 m0, s45
	s_nop 0
	global_load_lds_dwordx4 v[212:213], off
	s_waitcnt vmcnt(8)
	s_waitcnt lgkmcnt(0)
	s_setprio 1
	s_barrier
	v_mfma_i32_16x16x64_i8 v[60:63], v[76:79], v[180:183], v[60:63]
	v_mfma_i32_16x16x64_i8 v[56:59], v[84:87], v[180:183], v[56:59]
	v_mfma_i32_16x16x64_i8 v[44:47], v[76:79], v[188:191], v[44:47]
	v_mfma_i32_16x16x64_i8 v[40:43], v[84:87], v[188:191], v[40:43]
	v_mfma_i32_16x16x64_i8 v[28:31], v[76:79], v[196:199], v[28:31]
	v_mfma_i32_16x16x64_i8 v[24:27], v[84:87], v[196:199], v[24:27]
	v_mfma_i32_16x16x64_i8 v[12:15], v[76:79], v[204:207], v[12:15]
	v_mfma_i32_16x16x64_i8 v[8:11], v[84:87], v[204:207], v[8:11]
	v_mfma_i32_16x16x64_i8 v[60:63], v[80:83], v[184:187], v[60:63]
	v_mfma_i32_16x16x64_i8 v[56:59], v[88:91], v[184:187], v[56:59]
	v_mfma_i32_16x16x64_i8 v[44:47], v[80:83], v[192:195], v[44:47]
	v_mfma_i32_16x16x64_i8 v[40:43], v[88:91], v[192:195], v[40:43]
	v_mfma_i32_16x16x64_i8 v[28:31], v[80:83], v[200:203], v[28:31]
	v_mfma_i32_16x16x64_i8 v[24:27], v[88:91], v[200:203], v[24:27]
	v_mfma_i32_16x16x64_i8 v[12:15], v[80:83], v[208:211], v[12:15]
	v_mfma_i32_16x16x64_i8 v[8:11], v[88:91], v[208:211], v[8:11]
	v_mfma_i32_16x16x64_i8 v[52:55], v[160:163], v[180:183], v[52:55]
	v_mfma_i32_16x16x64_i8 v[48:51], v[172:175], v[180:183], v[48:51]
	v_mfma_i32_16x16x64_i8 v[36:39], v[160:163], v[188:191], v[36:39]
	v_mfma_i32_16x16x64_i8 v[32:35], v[172:175], v[188:191], v[32:35]
	v_mfma_i32_16x16x64_i8 v[20:23], v[160:163], v[196:199], v[20:23]
	v_mfma_i32_16x16x64_i8 v[16:19], v[172:175], v[196:199], v[16:19]
	v_mfma_i32_16x16x64_i8 v[4:7], v[160:163], v[204:207], v[4:7]
	v_mfma_i32_16x16x64_i8 v[0:3], v[172:175], v[204:207], v[0:3]
	v_mfma_i32_16x16x64_i8 v[52:55], v[168:171], v[184:187], v[52:55]
	v_mfma_i32_16x16x64_i8 v[48:51], v[176:179], v[184:187], v[48:51]
	v_mfma_i32_16x16x64_i8 v[36:39], v[168:171], v[192:195], v[36:39]
	v_mfma_i32_16x16x64_i8 v[32:35], v[176:179], v[192:195], v[32:35]
	v_mfma_i32_16x16x64_i8 v[20:23], v[168:171], v[200:203], v[20:23]
	v_mfma_i32_16x16x64_i8 v[16:19], v[176:179], v[200:203], v[16:19]
	v_mfma_i32_16x16x64_i8 v[4:7], v[168:171], v[208:211], v[4:7]
	v_mfma_i32_16x16x64_i8 v[0:3], v[176:179], v[208:211], v[0:3]
	s_barrier
	s_setprio 0
	s_add_i32 s50, s50, 2
	s_add_u32 s24, s24, 0x100
	s_addc_u32 s25, s25, 0
	s_add_u32 s15, s15, 0x100
	s_addc_u32 s17, s17, 0
	s_cmp_gt_u32 s50, 13
	s_cbranch_scc0 .LBB0_494

.LBB0_571:
	ds_read_b128 v[150:153], v137
	ds_read_b128 v[154:157], v137 offset:1024
	ds_read_b128 v[158:161], v137 offset:2048
	ds_read_b128 v[162:165], v137 offset:3072
	ds_read_b128 v[166:169], v144
	ds_read_b128 v[170:173], v144 offset:1024
	ds_read_b128 v[174:177], v144 offset:2048
	ds_read_b128 v[178:181], v144 offset:3072
	s_cmp_eq_u32 s69, 40
	s_cselect_b32 s30, s20, s61
	s_cselect_b32 s31, s21, s62
	s_cselect_b32 s28, s22, s63
	s_cselect_b32 s29, s23, s68
	s_add_u32 s26, s30, 0x80
	s_addc_u32 s27, s31, 0
	ds_read_b128 v[182:185], v145
	ds_read_b128 v[186:189], v145 offset:1024
	ds_read_b128 v[190:193], v145 offset:2048
	ds_read_b128 v[194:197], v145 offset:3072
	ds_read_b128 v[198:201], v145 offset:4096
	ds_read_b128 v[202:205], v145 offset:5120
	ds_read_b128 v[206:209], v145 offset:6144
	ds_read_b128 v[210:213], v145 offset:7168
	s_mov_b32 s70, m0
	s_mov_b32 m0, s55
	s_nop 0
	global_load_lds_dwordx4 v128, s[24:25]
	s_mov_b32 m0, s70
	s_nop 0
	s_mov_b32 s70, m0
	s_mov_b32 m0, s56
	s_nop 0
	global_load_lds_dwordx4 v130, s[24:25]
	s_mov_b32 m0, s70
	s_waitcnt vmcnt(8)
	s_waitcnt lgkmcnt(0)
	s_setprio 1
	s_barrier
	v_mfma_f32_16x16x128_f8f6f4 v[124:127], v[150:157], v[182:189], v[124:127]
	v_mfma_f32_16x16x128_f8f6f4 v[120:123], v[158:165], v[182:189], v[120:123]
	v_mfma_f32_16x16x128_f8f6f4 v[108:111], v[150:157], v[190:197], v[108:111]
	v_mfma_f32_16x16x128_f8f6f4 v[104:107], v[158:165], v[190:197], v[104:107]
	v_mfma_f32_16x16x128_f8f6f4 v[138:141], v[150:157], v[198:205], v[92:95]
	v_mfma_f32_16x16x128_f8f6f4 v[214:217], v[158:165], v[198:205], v[88:91]
	v_mfma_f32_16x16x128_f8f6f4 v[218:221], v[150:157], v[206:213], v[76:79]
	v_mfma_f32_16x16x128_f8f6f4 v[222:225], v[158:165], v[206:213], v[72:75]
	v_mfma_f32_16x16x128_f8f6f4 v[116:119], v[166:173], v[182:189], v[116:119]
	v_mfma_f32_16x16x128_f8f6f4 v[112:115], v[174:181], v[182:189], v[112:115]
	v_mfma_f32_16x16x128_f8f6f4 v[100:103], v[166:173], v[190:197], v[100:103]
	v_mfma_f32_16x16x128_f8f6f4 v[96:99], v[174:181], v[190:197], v[96:99]
	v_mfma_f32_16x16x128_f8f6f4 v[182:185], v[166:173], v[198:205], v[84:87]
	v_mfma_f32_16x16x128_f8f6f4 v[186:189], v[174:181], v[198:205], v[80:83]
	v_mfma_f32_16x16x128_f8f6f4 v[190:193], v[166:173], v[206:213], v[68:71]
	v_mfma_f32_16x16x128_f8f6f4 v[194:197], v[174:181], v[206:213], v[64:67]
	s_barrier
	s_setprio 0
	s_nop 4
	ds_read_b128 v[64:67], v145 offset:16384
	ds_read_b128 v[68:71], v145 offset:17408
	ds_read_b128 v[72:75], v145 offset:18432
	ds_read_b128 v[76:79], v145 offset:19456
	ds_read_b128 v[80:83], v145 offset:20480
	ds_read_b128 v[84:87], v145 offset:21504
	ds_read_b128 v[88:91], v145 offset:22528
	ds_read_b128 v[92:95], v145 offset:23552
	s_mov_b32 s70, m0
	s_mov_b32 m0, s39
	s_nop 0
	global_load_lds_dwordx4 v129, s[28:29]
	s_mov_b32 m0, s70
	s_nop 0
	s_mov_b32 s70, m0
	s_mov_b32 m0, s40
	s_nop 0
	global_load_lds_dwordx4 v131, s[28:29]
	s_mov_b32 m0, s70
	s_add_u32 s70, s28, 0xb0000
	s_addc_u32 s71, s29, 0
	s_mov_b32 s72, m0
	s_mov_b32 m0, s41
	s_nop 0
	global_load_lds_dwordx4 v129, s[70:71]
	s_mov_b32 m0, s72
	s_nop 0
	s_mov_b32 s72, m0
	s_mov_b32 m0, s42
	s_nop 0
	global_load_lds_dwordx4 v131, s[70:71]
	s_mov_b32 m0, s72
	s_mov_b32 s70, m0
	s_mov_b32 m0, s37
	s_nop 0
	global_load_lds_dwordx4 v128, s[30:31]
	s_mov_b32 m0, s70
	s_nop 0
	s_mov_b32 s70, m0
	s_mov_b32 m0, s43
	s_nop 0
	global_load_lds_dwordx4 v130, s[30:31]
	s_mov_b32 m0, s70
	s_waitcnt vmcnt(8)
	s_waitcnt lgkmcnt(0)
	s_setprio 1
	s_barrier
	v_mfma_f32_16x16x128_f8f6f4 v[60:63], v[150:157], v[64:71], v[60:63]
	v_mfma_f32_16x16x128_f8f6f4 v[56:59], v[158:165], v[64:71], v[56:59]
	v_mfma_f32_16x16x128_f8f6f4 v[198:201], v[150:157], v[72:79], v[44:47]
	v_mfma_f32_16x16x128_f8f6f4 v[202:205], v[158:165], v[72:79], v[40:43]
	v_mfma_f32_16x16x128_f8f6f4 v[206:209], v[150:157], v[80:87], v[28:31]
	v_mfma_f32_16x16x128_f8f6f4 v[210:213], v[158:165], v[80:87], v[24:27]
	v_mfma_f32_16x16x128_f8f6f4 v[226:229], v[150:157], v[88:95], v[12:15]
	v_mfma_f32_16x16x128_f8f6f4 v[230:233], v[158:165], v[88:95], v[8:11]
	v_mfma_f32_16x16x128_f8f6f4 v[52:55], v[166:173], v[64:71], v[52:55]
	v_mfma_f32_16x16x128_f8f6f4 v[48:51], v[174:181], v[64:71], v[48:51]
	v_mfma_f32_16x16x128_f8f6f4 v[234:237], v[166:173], v[72:79], v[36:39]
	v_mfma_f32_16x16x128_f8f6f4 v[238:241], v[174:181], v[72:79], v[32:35]
	v_mfma_f32_16x16x128_f8f6f4 v[242:245], v[166:173], v[80:87], v[20:23]
	v_mfma_f32_16x16x128_f8f6f4 v[246:249], v[174:181], v[80:87], v[16:19]
	v_mfma_f32_16x16x128_f8f6f4 v[250:253], v[166:173], v[88:95], v[4:7]
	v_mfma_f32_16x16x128_f8f6f4 v[132:135], v[174:181], v[88:95], v[0:3]
	s_barrier
	s_setprio 0
	s_nop 4
	ds_read_b128 v[0:3], v146
	ds_read_b128 v[4:7], v146 offset:1024
	ds_read_b128 v[16:19], v146 offset:2048
	ds_read_b128 v[20:23], v146 offset:3072
	ds_read_b128 v[150:153], v147
	ds_read_b128 v[154:157], v147 offset:1024
	ds_read_b128 v[158:161], v147 offset:2048
	ds_read_b128 v[162:165], v147 offset:3072
	ds_read_b128 v[8:11], v145 offset:32768
	ds_read_b128 v[12:15], v145 offset:33792
	ds_read_b128 v[24:27], v145 offset:34816
	ds_read_b128 v[28:31], v145 offset:35840
	ds_read_b128 v[32:35], v145 offset:36864
	ds_read_b128 v[36:39], v145 offset:37888
	ds_read_b128 v[40:43], v145 offset:38912
	ds_read_b128 v[44:47], v145 offset:39936
	s_add_u32 s30, s30, 0xb0000
	s_addc_u32 s31, s31, 0
	s_mov_b32 s70, m0
	s_mov_b32 m0, s44
	s_nop 0
	global_load_lds_dwordx4 v128, s[30:31]
	s_mov_b32 m0, s70
	s_nop 0
	s_mov_b32 s70, m0
	s_mov_b32 m0, s45
	s_nop 0
	global_load_lds_dwordx4 v130, s[30:31]
	s_mov_b32 m0, s70
	s_waitcnt vmcnt(8)
	s_waitcnt lgkmcnt(0)
	s_setprio 1
	s_barrier
	v_mfma_f32_16x16x128_f8f6f4 v[124:127], v[0:7], v[8:15], v[124:127]
	v_mfma_f32_16x16x128_f8f6f4 v[120:123], v[16:23], v[8:15], v[120:123]
	v_mfma_f32_16x16x128_f8f6f4 v[108:111], v[0:7], v[24:31], v[108:111]
	v_mfma_f32_16x16x128_f8f6f4 v[104:107], v[16:23], v[24:31], v[104:107]
	v_mfma_f32_16x16x128_f8f6f4 v[92:95], v[0:7], v[32:39], v[138:141]
	v_mfma_f32_16x16x128_f8f6f4 v[88:91], v[16:23], v[32:39], v[214:217]
	v_mfma_f32_16x16x128_f8f6f4 v[76:79], v[0:7], v[40:47], v[218:221]
	v_mfma_f32_16x16x128_f8f6f4 v[72:75], v[16:23], v[40:47], v[222:225]
	v_mfma_f32_16x16x128_f8f6f4 v[116:119], v[150:157], v[8:15], v[116:119]
	v_mfma_f32_16x16x128_f8f6f4 v[112:115], v[158:165], v[8:15], v[112:115]
	v_mfma_f32_16x16x128_f8f6f4 v[100:103], v[150:157], v[24:31], v[100:103]
	v_mfma_f32_16x16x128_f8f6f4 v[96:99], v[158:165], v[24:31], v[96:99]
	v_mfma_f32_16x16x128_f8f6f4 v[84:87], v[150:157], v[32:39], v[182:185]
	v_mfma_f32_16x16x128_f8f6f4 v[80:83], v[158:165], v[32:39], v[186:189]
	v_mfma_f32_16x16x128_f8f6f4 v[68:71], v[150:157], v[40:47], v[190:193]
	v_mfma_f32_16x16x128_f8f6f4 v[64:67], v[158:165], v[40:47], v[194:197]
	s_barrier
	s_setprio 0
	ds_read_b128 v[32:35], v145 offset:49152
	ds_read_b128 v[36:39], v145 offset:50176
	ds_read_b128 v[166:169], v145 offset:51200
	ds_read_b128 v[170:173], v145 offset:52224
	ds_read_b128 v[174:177], v145 offset:53248
	ds_read_b128 v[178:181], v145 offset:54272
	ds_read_b128 v[182:185], v145 offset:55296
	ds_read_b128 v[186:189], v145 offset:56320
	s_add_u32 s30, s28, 0x80
	s_addc_u32 s31, s29, 0
	s_mov_b32 s70, m0
	s_mov_b32 m0, s49
	s_nop 0
	global_load_lds_dwordx4 v129, s[30:31]
	s_mov_b32 m0, s70
	s_add_u32 s28, s28, 0xb0080
	s_mov_b32 s70, m0
	s_mov_b32 m0, s50
	s_nop 0
	global_load_lds_dwordx4 v131, s[30:31]
	s_mov_b32 m0, s70
	s_addc_u32 s29, s29, 0
	s_mov_b32 s30, m0
	s_mov_b32 m0, s53
	s_nop 0
	global_load_lds_dwordx4 v129, s[28:29]
	s_mov_b32 m0, s30
	s_nop 0
	s_mov_b32 s30, m0
	s_mov_b32 m0, s54
	s_nop 0
	global_load_lds_dwordx4 v131, s[28:29]
	s_mov_b32 m0, s30
	s_mov_b32 s28, m0
	s_mov_b32 m0, s51
	s_nop 0
	global_load_lds_dwordx4 v128, s[26:27]
	s_mov_b32 m0, s28
	s_nop 0
	s_mov_b32 s28, m0
	s_mov_b32 m0, s52
	s_nop 0
	global_load_lds_dwordx4 v130, s[26:27]
	s_mov_b32 m0, s28
	s_waitcnt vmcnt(8)
	s_waitcnt lgkmcnt(0)
	s_setprio 1
	s_barrier
	v_mfma_f32_16x16x128_f8f6f4 v[60:63], v[0:7], v[32:39], v[60:63]
	v_mfma_f32_16x16x128_f8f6f4 v[56:59], v[16:23], v[32:39], v[56:59]
	v_mfma_f32_16x16x128_f8f6f4 v[44:47], v[0:7], v[166:173], v[198:201]
	v_mfma_f32_16x16x128_f8f6f4 v[40:43], v[16:23], v[166:173], v[202:205]
	v_mfma_f32_16x16x128_f8f6f4 v[28:31], v[0:7], v[174:181], v[206:209]
	v_mfma_f32_16x16x128_f8f6f4 v[24:27], v[16:23], v[174:181], v[210:213]
	v_mfma_f32_16x16x128_f8f6f4 v[12:15], v[0:7], v[182:189], v[226:229]
	v_mfma_f32_16x16x128_f8f6f4 v[8:11], v[16:23], v[182:189], v[230:233]
	v_mfma_f32_16x16x128_f8f6f4 v[52:55], v[150:157], v[32:39], v[52:55]
	v_mfma_f32_16x16x128_f8f6f4 v[48:51], v[158:165], v[32:39], v[48:51]
	v_mfma_f32_16x16x128_f8f6f4 v[36:39], v[150:157], v[166:173], v[234:237]
	v_mfma_f32_16x16x128_f8f6f4 v[32:35], v[158:165], v[166:173], v[238:241]
	v_mfma_f32_16x16x128_f8f6f4 v[20:23], v[150:157], v[174:181], v[242:245]
	v_mfma_f32_16x16x128_f8f6f4 v[16:19], v[158:165], v[174:181], v[246:249]
	v_mfma_f32_16x16x128_f8f6f4 v[4:7], v[150:157], v[182:189], v[250:253]
	v_mfma_f32_16x16x128_f8f6f4 v[0:3], v[158:165], v[182:189], v[132:135]
	s_barrier
	s_setprio 0
	s_add_i32 s69, s69, 2
	s_add_u32 s61, s61, 0x100
	s_addc_u32 s62, s62, 0
	s_add_u32 s63, s63, 0x100
	s_addc_u32 s68, s68, 0
	s_add_u32 s24, s24, 0x100
	s_addc_u32 s25, s25, 0
	s_cmp_gt_u32 s69, 41
	s_cbranch_scc0 .LBB0_571
	s_and_b64 vcc, exec, s[10:11]
	s_cbranch_vccz .LBB0_574
	s_barrier

.LBB0_706:
	ds_read_b128 v[48:51], v181
	ds_read_b128 v[52:55], v181 offset:1024
	ds_read_b128 v[56:59], v181 offset:2048
	ds_read_b128 v[60:63], v181 offset:3072
	ds_read_b128 v[162:165], v182
	ds_read_b128 v[166:169], v182 offset:1024
	ds_read_b128 v[170:173], v182 offset:2048
	ds_read_b128 v[174:177], v182 offset:3072
	s_add_u32 s27, s28, 0xfffc0080
	s_addc_u32 s30, s29, -1
	s_cmp_eq_u32 s25, 12
	s_cselect_b32 s35, s21, s30
	s_cselect_b32 s34, s20, s27
	s_cselect_b32 s31, s23, s19
	s_cselect_b32 s30, s22, s17
	v_lshl_add_u64 v[178:179], s[28:29], 0, v[154:155]
	s_add_i32 m0, s40, 0xc000
	ds_read_b128 v[186:189], v183
	ds_read_b128 v[190:193], v183 offset:1024
	ds_read_b128 v[194:197], v183 offset:2048
	ds_read_b128 v[198:201], v183 offset:3072
	ds_read_b128 v[202:205], v183 offset:4096
	ds_read_b128 v[206:209], v183 offset:5120
	ds_read_b128 v[210:213], v183 offset:6144
	ds_read_b128 v[214:217], v183 offset:7168
	global_load_lds_dwordx4 v[178:179], off
	v_lshl_add_u64 v[178:179], s[28:29], 0, v[156:157]
	s_add_i32 m0, s40, 0xe000
	s_nop 0
	global_load_lds_dwordx4 v[178:179], off
	s_waitcnt vmcnt(8)
	s_waitcnt lgkmcnt(0)
	s_setprio 1
	s_barrier
	v_mfma_i32_16x16x64_i8 v[140:143], v[48:51], v[186:189], v[140:143]
	v_mfma_i32_16x16x64_i8 v[136:139], v[56:59], v[186:189], v[136:139]
	v_mfma_i32_16x16x64_i8 v[132:135], v[48:51], v[194:197], v[132:135]
	v_mfma_i32_16x16x64_i8 v[128:131], v[56:59], v[194:197], v[128:131]
	v_mfma_i32_16x16x64_i8 v[116:119], v[48:51], v[202:205], v[116:119]
	v_mfma_i32_16x16x64_i8 v[112:115], v[56:59], v[202:205], v[112:115]
	v_mfma_i32_16x16x64_i8 v[100:103], v[48:51], v[210:213], v[100:103]
	v_mfma_i32_16x16x64_i8 v[96:99], v[56:59], v[210:213], v[96:99]
	v_mfma_i32_16x16x64_i8 v[140:143], v[52:55], v[190:193], v[140:143]
	v_mfma_i32_16x16x64_i8 v[136:139], v[60:63], v[190:193], v[136:139]
	v_mfma_i32_16x16x64_i8 v[132:135], v[52:55], v[198:201], v[132:135]
	v_mfma_i32_16x16x64_i8 v[128:131], v[60:63], v[198:201], v[128:131]
	v_mfma_i32_16x16x64_i8 v[116:119], v[52:55], v[206:209], v[116:119]
	v_mfma_i32_16x16x64_i8 v[112:115], v[60:63], v[206:209], v[112:115]
	v_mfma_i32_16x16x64_i8 v[100:103], v[52:55], v[214:217], v[100:103]
	v_mfma_i32_16x16x64_i8 v[96:99], v[60:63], v[214:217], v[96:99]
	v_mfma_i32_16x16x64_i8 v[124:127], v[162:165], v[186:189], v[124:127]
	v_mfma_i32_16x16x64_i8 v[120:123], v[170:173], v[186:189], v[120:123]
	v_mfma_i32_16x16x64_i8 v[108:111], v[162:165], v[194:197], v[108:111]
	v_mfma_i32_16x16x64_i8 v[104:107], v[170:173], v[194:197], v[104:107]
	v_mfma_i32_16x16x64_i8 v[92:95], v[162:165], v[202:205], v[92:95]
	v_mfma_i32_16x16x64_i8 v[88:91], v[170:173], v[202:205], v[88:91]
	v_mfma_i32_16x16x64_i8 v[84:87], v[162:165], v[210:213], v[84:87]
	v_mfma_i32_16x16x64_i8 v[80:83], v[170:173], v[210:213], v[80:83]
	v_mfma_i32_16x16x64_i8 v[124:127], v[166:169], v[190:193], v[124:127]
	v_mfma_i32_16x16x64_i8 v[120:123], v[174:177], v[190:193], v[120:123]
	v_mfma_i32_16x16x64_i8 v[108:111], v[166:169], v[198:201], v[108:111]
	v_mfma_i32_16x16x64_i8 v[104:107], v[174:177], v[198:201], v[104:107]
	v_mfma_i32_16x16x64_i8 v[92:95], v[166:169], v[206:209], v[92:95]
	v_mfma_i32_16x16x64_i8 v[88:91], v[174:177], v[206:209], v[88:91]
	v_mfma_i32_16x16x64_i8 v[84:87], v[166:169], v[214:217], v[84:87]
	v_mfma_i32_16x16x64_i8 v[80:83], v[174:177], v[214:217], v[80:83]
	s_barrier
	s_setprio 0
	s_add_i32 s27, s54, s37
	v_lshl_add_u64 v[178:179], s[30:31], 0, v[148:149]
	s_mov_b32 m0, s27
	ds_read_b128 v[186:189], v183 offset:16384
	ds_read_b128 v[190:193], v183 offset:17408
	ds_read_b128 v[194:197], v183 offset:18432
	ds_read_b128 v[198:201], v183 offset:19456
	ds_read_b128 v[202:205], v183 offset:20480
	ds_read_b128 v[206:209], v183 offset:21504
	ds_read_b128 v[210:213], v183 offset:22528
	ds_read_b128 v[214:217], v183 offset:23552
	global_load_lds_dwordx4 v[178:179], off
	s_add_i32 m0, s27, 0x2000
	s_add_u32 s60, s30, 0x40000
	v_lshl_add_u64 v[218:219], s[30:31], 0, v[144:145]
	s_addc_u32 s61, s31, 0
	s_add_i32 s27, s55, s37
	global_load_lds_dwordx4 v[218:219], off
	v_lshl_add_u64 v[220:221], s[60:61], 0, v[148:149]
	s_mov_b32 m0, s27
	v_lshl_add_u64 v[222:223], s[34:35], 0, v[146:147]
	global_load_lds_dwordx4 v[220:221], off
	v_lshl_add_u64 v[220:221], s[60:61], 0, v[144:145]
	s_add_i32 m0, s27, 0x2000
	s_nop 0
	global_load_lds_dwordx4 v[220:221], off
	v_lshl_add_u64 v[220:221], s[34:35], 0, v[150:151]
	s_mov_b32 m0, s40
	s_nop 0
	global_load_lds_dwordx4 v[220:221], off
	s_mov_b32 m0, s41
	s_nop 0
	global_load_lds_dwordx4 v[222:223], off
	s_waitcnt vmcnt(8)
	s_waitcnt lgkmcnt(0)
	s_setprio 1
	s_barrier
	v_mfma_i32_16x16x64_i8 v[76:79], v[48:51], v[186:189], v[76:79]
	v_mfma_i32_16x16x64_i8 v[72:75], v[56:59], v[186:189], v[72:75]
	v_mfma_i32_16x16x64_i8 v[44:47], v[48:51], v[194:197], v[44:47]
	v_mfma_i32_16x16x64_i8 v[40:43], v[56:59], v[194:197], v[40:43]
	v_mfma_i32_16x16x64_i8 v[28:31], v[48:51], v[202:205], v[28:31]
	v_mfma_i32_16x16x64_i8 v[24:27], v[56:59], v[202:205], v[24:27]
	v_mfma_i32_16x16x64_i8 v[12:15], v[48:51], v[210:213], v[12:15]
	v_mfma_i32_16x16x64_i8 v[8:11], v[56:59], v[210:213], v[8:11]
	v_mfma_i32_16x16x64_i8 v[76:79], v[52:55], v[190:193], v[76:79]
	v_mfma_i32_16x16x64_i8 v[72:75], v[60:63], v[190:193], v[72:75]
	v_mfma_i32_16x16x64_i8 v[44:47], v[52:55], v[198:201], v[44:47]
	v_mfma_i32_16x16x64_i8 v[40:43], v[60:63], v[198:201], v[40:43]
	v_mfma_i32_16x16x64_i8 v[28:31], v[52:55], v[206:209], v[28:31]
	v_mfma_i32_16x16x64_i8 v[24:27], v[60:63], v[206:209], v[24:27]
	v_mfma_i32_16x16x64_i8 v[12:15], v[52:55], v[214:217], v[12:15]
	v_mfma_i32_16x16x64_i8 v[8:11], v[60:63], v[214:217], v[8:11]
	v_mfma_i32_16x16x64_i8 v[36:39], v[162:165], v[194:197], v[36:39]
	v_mfma_i32_16x16x64_i8 v[32:35], v[170:173], v[194:197], v[32:35]
	v_mfma_i32_16x16x64_i8 v[20:23], v[162:165], v[202:205], v[20:23]
	v_mfma_i32_16x16x64_i8 v[16:19], v[170:173], v[202:205], v[16:19]
	v_mfma_i32_16x16x64_i8 v[4:7], v[162:165], v[210:213], v[4:7]
	v_mfma_i32_16x16x64_i8 v[0:3], v[170:173], v[210:213], v[0:3]
	v_mfma_i32_16x16x64_i8 v[48:51], v[162:165], v[186:189], v[68:71]
	v_mfma_i32_16x16x64_i8 v[52:55], v[170:173], v[186:189], v[64:67]
	v_mfma_i32_16x16x64_i8 v[36:39], v[166:169], v[198:201], v[36:39]
	v_mfma_i32_16x16x64_i8 v[32:35], v[174:177], v[198:201], v[32:35]
	v_mfma_i32_16x16x64_i8 v[20:23], v[166:169], v[206:209], v[20:23]
	v_mfma_i32_16x16x64_i8 v[16:19], v[174:177], v[206:209], v[16:19]
	v_mfma_i32_16x16x64_i8 v[4:7], v[166:169], v[214:217], v[4:7]
	v_mfma_i32_16x16x64_i8 v[0:3], v[174:177], v[214:217], v[0:3]
	v_mfma_i32_16x16x64_i8 v[48:51], v[166:169], v[190:193], v[48:51]
	v_mfma_i32_16x16x64_i8 v[52:55], v[174:177], v[190:193], v[52:55]
	s_barrier
	s_setprio 0
	s_add_i32 s27, 0, 0x18000
	s_add_i32 s60, 0, 0x1c000
	v_add_u32_e32 v68, s27, v180
	v_add_u32_e32 v152, s60, v180
	ds_read_b128 v[56:59], v68
	ds_read_b128 v[60:63], v68 offset:1024
	ds_read_b128 v[64:67], v68 offset:2048
	ds_read_b128 v[68:71], v68 offset:3072
	ds_read_b128 v[162:165], v152
	ds_read_b128 v[166:169], v152 offset:1024
	ds_read_b128 v[170:173], v152 offset:2048
	ds_read_b128 v[174:177], v152 offset:3072
	s_add_u32 s34, s34, 0x40000
	s_addc_u32 s35, s35, 0
	s_mov_b32 m0, s42
	v_lshl_add_u64 v[224:225], s[34:35], 0, v[150:151]
	ds_read_b128 v[186:189], v183 offset:32768
	ds_read_b128 v[190:193], v183 offset:33792
	ds_read_b128 v[194:197], v183 offset:34816
	ds_read_b128 v[198:201], v183 offset:35840
	ds_read_b128 v[202:205], v183 offset:36864
	ds_read_b128 v[206:209], v183 offset:37888
	ds_read_b128 v[210:213], v183 offset:38912
	ds_read_b128 v[214:217], v183 offset:39936
	global_load_lds_dwordx4 v[224:225], off
	v_lshl_add_u64 v[224:225], s[34:35], 0, v[146:147]
	s_mov_b32 m0, s43
	s_nop 0
	global_load_lds_dwordx4 v[224:225], off
	s_waitcnt vmcnt(8)
	s_waitcnt lgkmcnt(0)
	s_setprio 1
	s_barrier
	v_mfma_i32_16x16x64_i8 v[140:143], v[56:59], v[186:189], v[140:143]
	v_mfma_i32_16x16x64_i8 v[136:139], v[64:67], v[186:189], v[136:139]
	v_mfma_i32_16x16x64_i8 v[132:135], v[56:59], v[194:197], v[132:135]
	v_mfma_i32_16x16x64_i8 v[128:131], v[64:67], v[194:197], v[128:131]
	v_mfma_i32_16x16x64_i8 v[116:119], v[56:59], v[202:205], v[116:119]
	v_mfma_i32_16x16x64_i8 v[112:115], v[64:67], v[202:205], v[112:115]
	v_mfma_i32_16x16x64_i8 v[100:103], v[56:59], v[210:213], v[100:103]
	v_mfma_i32_16x16x64_i8 v[96:99], v[64:67], v[210:213], v[96:99]
	v_mfma_i32_16x16x64_i8 v[140:143], v[60:63], v[190:193], v[140:143]
	v_mfma_i32_16x16x64_i8 v[136:139], v[68:71], v[190:193], v[136:139]
	v_mfma_i32_16x16x64_i8 v[132:135], v[60:63], v[198:201], v[132:135]
	v_mfma_i32_16x16x64_i8 v[128:131], v[68:71], v[198:201], v[128:131]
	v_mfma_i32_16x16x64_i8 v[116:119], v[60:63], v[206:209], v[116:119]
	v_mfma_i32_16x16x64_i8 v[112:115], v[68:71], v[206:209], v[112:115]
	v_mfma_i32_16x16x64_i8 v[100:103], v[60:63], v[214:217], v[100:103]
	v_mfma_i32_16x16x64_i8 v[96:99], v[68:71], v[214:217], v[96:99]
	v_mfma_i32_16x16x64_i8 v[124:127], v[162:165], v[186:189], v[124:127]
	v_mfma_i32_16x16x64_i8 v[120:123], v[170:173], v[186:189], v[120:123]
	v_mfma_i32_16x16x64_i8 v[108:111], v[162:165], v[194:197], v[108:111]
	v_mfma_i32_16x16x64_i8 v[104:107], v[170:173], v[194:197], v[104:107]
	v_mfma_i32_16x16x64_i8 v[92:95], v[162:165], v[202:205], v[92:95]
	v_mfma_i32_16x16x64_i8 v[88:91], v[170:173], v[202:205], v[88:91]
	v_mfma_i32_16x16x64_i8 v[84:87], v[162:165], v[210:213], v[84:87]
	v_mfma_i32_16x16x64_i8 v[80:83], v[170:173], v[210:213], v[80:83]
	v_mfma_i32_16x16x64_i8 v[124:127], v[166:169], v[190:193], v[124:127]
	v_mfma_i32_16x16x64_i8 v[120:123], v[174:177], v[190:193], v[120:123]
	v_mfma_i32_16x16x64_i8 v[108:111], v[166:169], v[198:201], v[108:111]
	v_mfma_i32_16x16x64_i8 v[104:107], v[174:177], v[198:201], v[104:107]
	v_mfma_i32_16x16x64_i8 v[92:95], v[166:169], v[206:209], v[92:95]
	v_mfma_i32_16x16x64_i8 v[88:91], v[174:177], v[206:209], v[88:91]
	v_mfma_i32_16x16x64_i8 v[84:87], v[166:169], v[214:217], v[84:87]
	v_mfma_i32_16x16x64_i8 v[80:83], v[174:177], v[214:217], v[80:83]
	s_barrier
	s_setprio 0
	s_add_i32 s27, s27, s37
	v_lshl_add_u64 v[178:179], v[178:179], 0, s[14:15]
	s_mov_b32 m0, s27
	ds_read_b128 v[186:189], v183 offset:49152
	ds_read_b128 v[190:193], v183 offset:50176
	ds_read_b128 v[194:197], v183 offset:51200
	ds_read_b128 v[198:201], v183 offset:52224
	ds_read_b128 v[202:205], v183 offset:53248
	ds_read_b128 v[206:209], v183 offset:54272
	ds_read_b128 v[210:213], v183 offset:55296
	ds_read_b128 v[214:217], v183 offset:56320
	global_load_lds_dwordx4 v[178:179], off
	s_add_i32 m0, s27, 0x2000
	s_add_u32 s30, s30, 0x40080
	v_lshl_add_u64 v[178:179], v[218:219], 0, s[14:15]
	s_addc_u32 s31, s31, 0
	s_add_i32 s27, s60, s37
	global_load_lds_dwordx4 v[178:179], off
	v_lshl_add_u64 v[178:179], s[30:31], 0, v[148:149]
	s_mov_b32 m0, s27
	s_nop 0
	global_load_lds_dwordx4 v[178:179], off
	v_lshl_add_u64 v[178:179], s[30:31], 0, v[144:145]
	s_add_i32 m0, s27, 0x2000
	s_nop 0
	global_load_lds_dwordx4 v[178:179], off
	v_lshl_add_u64 v[178:179], v[220:221], 0, s[14:15]
	s_mov_b32 m0, s52
	s_nop 0
	global_load_lds_dwordx4 v[178:179], off
	v_lshl_add_u64 v[178:179], v[222:223], 0, s[14:15]
	s_mov_b32 m0, s53
	s_nop 0
	global_load_lds_dwordx4 v[178:179], off
	s_waitcnt vmcnt(8)
	s_waitcnt lgkmcnt(0)
	s_setprio 1
	s_barrier
	v_mfma_i32_16x16x64_i8 v[76:79], v[56:59], v[186:189], v[76:79]
	v_mfma_i32_16x16x64_i8 v[72:75], v[64:67], v[186:189], v[72:75]
	v_mfma_i32_16x16x64_i8 v[44:47], v[56:59], v[194:197], v[44:47]
	v_mfma_i32_16x16x64_i8 v[40:43], v[64:67], v[194:197], v[40:43]
	v_mfma_i32_16x16x64_i8 v[28:31], v[56:59], v[202:205], v[28:31]
	v_mfma_i32_16x16x64_i8 v[24:27], v[64:67], v[202:205], v[24:27]
	v_mfma_i32_16x16x64_i8 v[12:15], v[56:59], v[210:213], v[12:15]
	v_mfma_i32_16x16x64_i8 v[8:11], v[64:67], v[210:213], v[8:11]
	v_mfma_i32_16x16x64_i8 v[76:79], v[60:63], v[190:193], v[76:79]
	v_mfma_i32_16x16x64_i8 v[72:75], v[68:71], v[190:193], v[72:75]
	v_mfma_i32_16x16x64_i8 v[44:47], v[60:63], v[198:201], v[44:47]
	v_mfma_i32_16x16x64_i8 v[40:43], v[68:71], v[198:201], v[40:43]
	v_mfma_i32_16x16x64_i8 v[28:31], v[60:63], v[206:209], v[28:31]
	v_mfma_i32_16x16x64_i8 v[24:27], v[68:71], v[206:209], v[24:27]
	v_mfma_i32_16x16x64_i8 v[12:15], v[60:63], v[214:217], v[12:15]
	v_mfma_i32_16x16x64_i8 v[8:11], v[68:71], v[214:217], v[8:11]
	v_mfma_i32_16x16x64_i8 v[48:51], v[162:165], v[186:189], v[48:51]
	v_mfma_i32_16x16x64_i8 v[68:71], v[166:169], v[190:193], v[48:51]
	v_mfma_i32_16x16x64_i8 v[48:51], v[170:173], v[186:189], v[52:55]
	v_mfma_i32_16x16x64_i8 v[36:39], v[162:165], v[194:197], v[36:39]
	v_mfma_i32_16x16x64_i8 v[32:35], v[170:173], v[194:197], v[32:35]
	v_mfma_i32_16x16x64_i8 v[20:23], v[162:165], v[202:205], v[20:23]
	v_mfma_i32_16x16x64_i8 v[16:19], v[170:173], v[202:205], v[16:19]
	v_mfma_i32_16x16x64_i8 v[4:7], v[162:165], v[210:213], v[4:7]
	v_mfma_i32_16x16x64_i8 v[0:3], v[170:173], v[210:213], v[0:3]
	v_mfma_i32_16x16x64_i8 v[64:67], v[174:177], v[190:193], v[48:51]
	v_mfma_i32_16x16x64_i8 v[36:39], v[166:169], v[198:201], v[36:39]
	v_mfma_i32_16x16x64_i8 v[32:35], v[174:177], v[198:201], v[32:35]
	v_mfma_i32_16x16x64_i8 v[20:23], v[166:169], v[206:209], v[20:23]
	v_mfma_i32_16x16x64_i8 v[16:19], v[174:177], v[206:209], v[16:19]
	v_mfma_i32_16x16x64_i8 v[4:7], v[166:169], v[214:217], v[4:7]
	v_mfma_i32_16x16x64_i8 v[0:3], v[174:177], v[214:217], v[0:3]
	s_barrier
	s_setprio 0
	s_add_i32 s25, s25, 2
	s_add_u32 s28, s28, 0x100
	s_addc_u32 s29, s29, 0
	s_add_u32 s17, s17, 0x100
	s_addc_u32 s19, s19, 0
	s_cmp_gt_u32 s25, 13
	s_cbranch_scc0 .LBB0_706
	s_and_b64 vcc, exec, s[12:13]
	s_cbranch_vccz .LBB0_709
	s_barrier

.LBB0_1622:
	ds_read_b128 v[150:153], v143
	ds_read_b128 v[154:157], v143 offset:1024
	ds_read_b128 v[158:161], v143 offset:2048
	ds_read_b128 v[162:165], v143 offset:3072
	ds_read_b128 v[166:169], v144
	ds_read_b128 v[170:173], v144 offset:1024
	ds_read_b128 v[174:177], v144 offset:2048
	ds_read_b128 v[178:181], v144 offset:3072
	s_cmp_eq_u32 s69, 12
	s_cselect_b32 s40, s24, s21
	s_cselect_b32 s41, s25, s23
	s_cselect_b32 s38, s26, s63
	s_cselect_b32 s39, s27, s68
	s_add_u32 s36, s40, 0x80
	s_addc_u32 s37, s41, 0
	ds_read_b128 v[182:185], v145
	ds_read_b128 v[186:189], v145 offset:1024
	ds_read_b128 v[190:193], v145 offset:2048
	ds_read_b128 v[194:197], v145 offset:3072
	ds_read_b128 v[198:201], v145 offset:4096
	ds_read_b128 v[202:205], v145 offset:5120
	ds_read_b128 v[206:209], v145 offset:6144
	ds_read_b128 v[210:213], v145 offset:7168
	s_mov_b32 s70, m0
	s_mov_b32 m0, s61
	s_nop 0
	global_load_lds_dwordx4 v133, s[34:35]
	s_mov_b32 m0, s70
	s_nop 0
	s_mov_b32 s70, m0
	s_mov_b32 m0, s62
	s_nop 0
	global_load_lds_dwordx4 v141, s[34:35]
	s_mov_b32 m0, s70
	s_waitcnt vmcnt(8)
	s_waitcnt lgkmcnt(0)
	s_setprio 1
	s_barrier
	v_mfma_f32_16x16x128_f8f6f4 v[124:127], v[150:157], v[182:189], v[124:127]
	v_mfma_f32_16x16x128_f8f6f4 v[120:123], v[158:165], v[182:189], v[120:123]
	v_mfma_f32_16x16x128_f8f6f4 v[108:111], v[150:157], v[190:197], v[108:111]
	v_mfma_f32_16x16x128_f8f6f4 v[104:107], v[158:165], v[190:197], v[104:107]
	v_mfma_f32_16x16x128_f8f6f4 v[134:137], v[150:157], v[198:205], v[92:95]
	v_mfma_f32_16x16x128_f8f6f4 v[214:217], v[158:165], v[198:205], v[88:91]
	v_mfma_f32_16x16x128_f8f6f4 v[218:221], v[150:157], v[206:213], v[76:79]
	v_mfma_f32_16x16x128_f8f6f4 v[222:225], v[158:165], v[206:213], v[72:75]
	v_mfma_f32_16x16x128_f8f6f4 v[116:119], v[166:173], v[182:189], v[116:119]
	v_mfma_f32_16x16x128_f8f6f4 v[112:115], v[174:181], v[182:189], v[112:115]
	v_mfma_f32_16x16x128_f8f6f4 v[100:103], v[166:173], v[190:197], v[100:103]
	v_mfma_f32_16x16x128_f8f6f4 v[96:99], v[174:181], v[190:197], v[96:99]
	v_mfma_f32_16x16x128_f8f6f4 v[182:185], v[166:173], v[198:205], v[84:87]
	v_mfma_f32_16x16x128_f8f6f4 v[186:189], v[174:181], v[198:205], v[80:83]
	v_mfma_f32_16x16x128_f8f6f4 v[190:193], v[166:173], v[206:213], v[68:71]
	v_mfma_f32_16x16x128_f8f6f4 v[194:197], v[174:181], v[206:213], v[64:67]
	s_barrier
	s_setprio 0
	s_nop 4
	ds_read_b128 v[64:67], v145 offset:16384
	ds_read_b128 v[68:71], v145 offset:17408
	ds_read_b128 v[72:75], v145 offset:18432
	ds_read_b128 v[76:79], v145 offset:19456
	ds_read_b128 v[80:83], v145 offset:20480
	ds_read_b128 v[84:87], v145 offset:21504
	ds_read_b128 v[88:91], v145 offset:22528
	ds_read_b128 v[92:95], v145 offset:23552
	s_mov_b32 s70, m0
	s_mov_b32 m0, s29
	s_nop 0
	global_load_lds_dwordx4 v140, s[38:39]
	s_mov_b32 m0, s70
	s_nop 0
	s_mov_b32 s70, m0
	s_mov_b32 m0, s31
	s_nop 0
	global_load_lds_dwordx4 v142, s[38:39]
	s_mov_b32 m0, s70
	s_add_u32 s70, s38, 0x40000
	s_addc_u32 s71, s39, 0
	s_mov_b32 s72, m0
	s_mov_b32 m0, s47
	s_nop 0
	global_load_lds_dwordx4 v140, s[70:71]
	s_mov_b32 m0, s72
	s_nop 0
	s_mov_b32 s72, m0
	s_mov_b32 m0, s48
	s_nop 0
	global_load_lds_dwordx4 v142, s[70:71]
	s_mov_b32 m0, s72
	s_mov_b32 s70, m0
	s_mov_b32 m0, s45
	s_nop 0
	global_load_lds_dwordx4 v133, s[40:41]
	s_mov_b32 m0, s70
	s_nop 0
	s_mov_b32 s70, m0
	s_mov_b32 m0, s49
	s_nop 0
	global_load_lds_dwordx4 v141, s[40:41]
	s_mov_b32 m0, s70
	s_waitcnt vmcnt(8)
	s_waitcnt lgkmcnt(0)
	s_setprio 1
	s_barrier
	v_mfma_f32_16x16x128_f8f6f4 v[60:63], v[150:157], v[64:71], v[60:63]
	v_mfma_f32_16x16x128_f8f6f4 v[56:59], v[158:165], v[64:71], v[56:59]
	v_mfma_f32_16x16x128_f8f6f4 v[198:201], v[150:157], v[72:79], v[44:47]
	v_mfma_f32_16x16x128_f8f6f4 v[202:205], v[158:165], v[72:79], v[40:43]
	v_mfma_f32_16x16x128_f8f6f4 v[206:209], v[150:157], v[80:87], v[28:31]
	v_mfma_f32_16x16x128_f8f6f4 v[210:213], v[158:165], v[80:87], v[24:27]
	v_mfma_f32_16x16x128_f8f6f4 v[226:229], v[150:157], v[88:95], v[12:15]
	v_mfma_f32_16x16x128_f8f6f4 v[230:233], v[158:165], v[88:95], v[8:11]
	v_mfma_f32_16x16x128_f8f6f4 v[52:55], v[166:173], v[64:71], v[52:55]
	v_mfma_f32_16x16x128_f8f6f4 v[48:51], v[174:181], v[64:71], v[48:51]
	v_mfma_f32_16x16x128_f8f6f4 v[234:237], v[166:173], v[72:79], v[36:39]
	v_mfma_f32_16x16x128_f8f6f4 v[238:241], v[174:181], v[72:79], v[32:35]
	v_mfma_f32_16x16x128_f8f6f4 v[242:245], v[166:173], v[80:87], v[20:23]
	v_mfma_f32_16x16x128_f8f6f4 v[246:249], v[174:181], v[80:87], v[16:19]
	v_mfma_f32_16x16x128_f8f6f4 v[250:253], v[166:173], v[88:95], v[4:7]
	v_mfma_f32_16x16x128_f8f6f4 v[128:131], v[174:181], v[88:95], v[0:3]
	s_barrier
	s_setprio 0
	s_nop 4
	ds_read_b128 v[0:3], v146
	ds_read_b128 v[4:7], v146 offset:1024
	ds_read_b128 v[16:19], v146 offset:2048
	ds_read_b128 v[20:23], v146 offset:3072
	ds_read_b128 v[150:153], v147
	ds_read_b128 v[154:157], v147 offset:1024
	ds_read_b128 v[158:161], v147 offset:2048
	ds_read_b128 v[162:165], v147 offset:3072
	ds_read_b128 v[8:11], v145 offset:32768
	ds_read_b128 v[12:15], v145 offset:33792
	ds_read_b128 v[24:27], v145 offset:34816
	ds_read_b128 v[28:31], v145 offset:35840
	ds_read_b128 v[32:35], v145 offset:36864
	ds_read_b128 v[36:39], v145 offset:37888
	ds_read_b128 v[40:43], v145 offset:38912
	ds_read_b128 v[44:47], v145 offset:39936
	s_add_u32 s40, s40, 0x40000
	s_addc_u32 s41, s41, 0
	s_mov_b32 s70, m0
	s_mov_b32 m0, s50
	s_nop 0
	global_load_lds_dwordx4 v133, s[40:41]
	s_mov_b32 m0, s70
	s_nop 0
	s_mov_b32 s70, m0
	s_mov_b32 m0, s51
	s_nop 0
	global_load_lds_dwordx4 v141, s[40:41]
	s_mov_b32 m0, s70
	s_waitcnt vmcnt(8)
	s_waitcnt lgkmcnt(0)
	s_setprio 1
	s_barrier
	v_mfma_f32_16x16x128_f8f6f4 v[124:127], v[0:7], v[8:15], v[124:127]
	v_mfma_f32_16x16x128_f8f6f4 v[120:123], v[16:23], v[8:15], v[120:123]
	v_mfma_f32_16x16x128_f8f6f4 v[108:111], v[0:7], v[24:31], v[108:111]
	v_mfma_f32_16x16x128_f8f6f4 v[104:107], v[16:23], v[24:31], v[104:107]
	v_mfma_f32_16x16x128_f8f6f4 v[92:95], v[0:7], v[32:39], v[134:137]
	v_mfma_f32_16x16x128_f8f6f4 v[88:91], v[16:23], v[32:39], v[214:217]
	v_mfma_f32_16x16x128_f8f6f4 v[76:79], v[0:7], v[40:47], v[218:221]
	v_mfma_f32_16x16x128_f8f6f4 v[72:75], v[16:23], v[40:47], v[222:225]
	v_mfma_f32_16x16x128_f8f6f4 v[116:119], v[150:157], v[8:15], v[116:119]
	v_mfma_f32_16x16x128_f8f6f4 v[112:115], v[158:165], v[8:15], v[112:115]
	v_mfma_f32_16x16x128_f8f6f4 v[100:103], v[150:157], v[24:31], v[100:103]
	v_mfma_f32_16x16x128_f8f6f4 v[96:99], v[158:165], v[24:31], v[96:99]
	v_mfma_f32_16x16x128_f8f6f4 v[84:87], v[150:157], v[32:39], v[182:185]
	v_mfma_f32_16x16x128_f8f6f4 v[80:83], v[158:165], v[32:39], v[186:189]
	v_mfma_f32_16x16x128_f8f6f4 v[68:71], v[150:157], v[40:47], v[190:193]
	v_mfma_f32_16x16x128_f8f6f4 v[64:67], v[158:165], v[40:47], v[194:197]
	s_barrier
	s_setprio 0
	ds_read_b128 v[32:35], v145 offset:49152
	ds_read_b128 v[36:39], v145 offset:50176
	ds_read_b128 v[166:169], v145 offset:51200
	ds_read_b128 v[170:173], v145 offset:52224
	ds_read_b128 v[174:177], v145 offset:53248
	ds_read_b128 v[178:181], v145 offset:54272
	ds_read_b128 v[182:185], v145 offset:55296
	ds_read_b128 v[186:189], v145 offset:56320
	s_add_u32 s40, s38, 0x80
	s_addc_u32 s41, s39, 0
	s_mov_b32 s70, m0
	s_mov_b32 m0, s55
	s_nop 0
	global_load_lds_dwordx4 v140, s[40:41]
	s_mov_b32 m0, s70
	s_add_u32 s38, s38, 0x40080
	s_mov_b32 s70, m0
	s_mov_b32 m0, s56
	s_nop 0
	global_load_lds_dwordx4 v142, s[40:41]
	s_mov_b32 m0, s70
	s_addc_u32 s39, s39, 0
	s_mov_b32 s40, m0
	s_mov_b32 m0, s59
	s_nop 0
	global_load_lds_dwordx4 v140, s[38:39]
	s_mov_b32 m0, s40
	s_nop 0
	s_mov_b32 s40, m0
	s_mov_b32 m0, s60
	s_nop 0
	global_load_lds_dwordx4 v142, s[38:39]
	s_mov_b32 m0, s40
	s_mov_b32 s38, m0
	s_mov_b32 m0, s57
	s_nop 0
	global_load_lds_dwordx4 v133, s[36:37]
	s_mov_b32 m0, s38
	s_nop 0
	s_mov_b32 s38, m0
	s_mov_b32 m0, s58
	s_nop 0
	global_load_lds_dwordx4 v141, s[36:37]
	s_mov_b32 m0, s38
	s_waitcnt vmcnt(8)
	s_waitcnt lgkmcnt(0)
	s_setprio 1
	s_barrier
	v_mfma_f32_16x16x128_f8f6f4 v[60:63], v[0:7], v[32:39], v[60:63]
	v_mfma_f32_16x16x128_f8f6f4 v[56:59], v[16:23], v[32:39], v[56:59]
	v_mfma_f32_16x16x128_f8f6f4 v[44:47], v[0:7], v[166:173], v[198:201]
	v_mfma_f32_16x16x128_f8f6f4 v[40:43], v[16:23], v[166:173], v[202:205]
	v_mfma_f32_16x16x128_f8f6f4 v[28:31], v[0:7], v[174:181], v[206:209]
	v_mfma_f32_16x16x128_f8f6f4 v[24:27], v[16:23], v[174:181], v[210:213]
	v_mfma_f32_16x16x128_f8f6f4 v[12:15], v[0:7], v[182:189], v[226:229]
	v_mfma_f32_16x16x128_f8f6f4 v[8:11], v[16:23], v[182:189], v[230:233]
	v_mfma_f32_16x16x128_f8f6f4 v[52:55], v[150:157], v[32:39], v[52:55]
	v_mfma_f32_16x16x128_f8f6f4 v[48:51], v[158:165], v[32:39], v[48:51]
	v_mfma_f32_16x16x128_f8f6f4 v[36:39], v[150:157], v[166:173], v[234:237]
	v_mfma_f32_16x16x128_f8f6f4 v[32:35], v[158:165], v[166:173], v[238:241]
	v_mfma_f32_16x16x128_f8f6f4 v[20:23], v[150:157], v[174:181], v[242:245]
	v_mfma_f32_16x16x128_f8f6f4 v[16:19], v[158:165], v[174:181], v[246:249]
	v_mfma_f32_16x16x128_f8f6f4 v[4:7], v[150:157], v[182:189], v[250:253]
	v_mfma_f32_16x16x128_f8f6f4 v[0:3], v[158:165], v[182:189], v[128:131]
	s_barrier
	s_setprio 0
	s_add_i32 s69, s69, 2
	s_add_u32 s21, s21, 0x100
	s_addc_u32 s23, s23, 0
	s_add_u32 s63, s63, 0x100
	s_addc_u32 s68, s68, 0
	s_add_u32 s34, s34, 0x100
	s_addc_u32 s35, s35, 0
	s_cmp_gt_u32 s69, 13
	s_cbranch_scc0 .LBB0_1622
	s_and_b64 vcc, exec, s[8:9]
	s_cbranch_vccz .LBB0_1625
	s_barrier

.LBB0_1847:
	s_add_u32 s28, s28, 0x40080
	s_addc_u32 s29, s29, 0
	s_add_u32 s17, s30, 0x100
	s_addc_u32 s19, s31, 0
	s_mov_b32 s69, -2
	ds_read_b128 v[76:79], v163
	ds_read_b128 v[80:83], v163 offset:1024
	ds_read_b128 v[84:87], v163 offset:2048
	ds_read_b128 v[88:91], v163 offset:3072
	ds_read_b128 v[158:161], v164
	ds_read_b128 v[166:169], v164 offset:1024
	ds_read_b128 v[170:173], v164 offset:2048
	ds_read_b128 v[174:177], v164 offset:3072
	s_add_u32 s30, s28, 0xfffc0080
	s_addc_u32 s31, s29, -1
	s_cmp_eq_u32 s69, 12
	s_cselect_b32 s35, s21, s31
	s_cselect_b32 s34, s20, s30
	s_cselect_b32 s31, s23, s19
	s_cselect_b32 s30, s22, s17
	v_lshl_add_u64 v[210:211], s[28:29], 0, v[152:153]
	s_add_i32 m0, s25, 0xc000
	ds_read_b128 v[178:181], v165
	ds_read_b128 v[182:185], v165 offset:1024
	ds_read_b128 v[186:189], v165 offset:2048
	ds_read_b128 v[190:193], v165 offset:3072
	ds_read_b128 v[194:197], v165 offset:4096
	ds_read_b128 v[198:201], v165 offset:5120
	ds_read_b128 v[202:205], v165 offset:6144
	ds_read_b128 v[206:209], v165 offset:7168
	global_load_lds_dwordx4 v[210:211], off
	v_lshl_add_u64 v[210:211], s[28:29], 0, v[154:155]
	s_add_i32 m0, s25, 0xe000
	s_nop 0
	global_load_lds_dwordx4 v[210:211], off
	s_waitcnt vmcnt(8)
	s_waitcnt lgkmcnt(0)
	s_setprio 1
	s_barrier
	v_mfma_i32_16x16x64_i8 v[140:143], v[76:79], v[178:181], 0
	v_mfma_i32_16x16x64_i8 v[136:139], v[84:87], v[178:181], 0
	v_mfma_i32_16x16x64_i8 v[124:127], v[76:79], v[186:189], 0
	v_mfma_i32_16x16x64_i8 v[120:123], v[84:87], v[186:189], 0
	v_mfma_i32_16x16x64_i8 v[108:111], v[76:79], v[194:197], 0
	v_mfma_i32_16x16x64_i8 v[104:107], v[84:87], v[194:197], 0
	v_mfma_i32_16x16x64_i8 v[92:95], v[76:79], v[202:205], 0
	v_mfma_i32_16x16x64_i8 v[72:75], v[84:87], v[202:205], 0
	v_mfma_i32_16x16x64_i8 v[140:143], v[80:83], v[182:185], v[140:143]
	v_mfma_i32_16x16x64_i8 v[136:139], v[88:91], v[182:185], v[136:139]
	v_mfma_i32_16x16x64_i8 v[124:127], v[80:83], v[190:193], v[124:127]
	v_mfma_i32_16x16x64_i8 v[120:123], v[88:91], v[190:193], v[120:123]
	v_mfma_i32_16x16x64_i8 v[108:111], v[80:83], v[198:201], v[108:111]
	v_mfma_i32_16x16x64_i8 v[104:107], v[88:91], v[198:201], v[104:107]
	v_mfma_i32_16x16x64_i8 v[92:95], v[80:83], v[206:209], v[92:95]
	v_mfma_i32_16x16x64_i8 v[72:75], v[88:91], v[206:209], v[72:75]
	v_mfma_i32_16x16x64_i8 v[132:135], v[158:161], v[178:181], 0
	v_mfma_i32_16x16x64_i8 v[128:131], v[170:173], v[178:181], 0
	v_mfma_i32_16x16x64_i8 v[116:119], v[158:161], v[186:189], 0
	v_mfma_i32_16x16x64_i8 v[112:115], v[170:173], v[186:189], 0
	v_mfma_i32_16x16x64_i8 v[100:103], v[158:161], v[194:197], 0
	v_mfma_i32_16x16x64_i8 v[96:99], v[170:173], v[194:197], 0
	v_mfma_i32_16x16x64_i8 v[68:71], v[158:161], v[202:205], 0
	v_mfma_i32_16x16x64_i8 v[64:67], v[170:173], v[202:205], 0
	v_mfma_i32_16x16x64_i8 v[132:135], v[166:169], v[182:185], v[132:135]
	v_mfma_i32_16x16x64_i8 v[128:131], v[174:177], v[182:185], v[128:131]
	v_mfma_i32_16x16x64_i8 v[116:119], v[166:169], v[190:193], v[116:119]
	v_mfma_i32_16x16x64_i8 v[112:115], v[174:177], v[190:193], v[112:115]
	v_mfma_i32_16x16x64_i8 v[100:103], v[166:169], v[198:201], v[100:103]
	v_mfma_i32_16x16x64_i8 v[96:99], v[174:177], v[198:201], v[96:99]
	v_mfma_i32_16x16x64_i8 v[68:71], v[166:169], v[206:209], v[68:71]
	v_mfma_i32_16x16x64_i8 v[64:67], v[174:177], v[206:209], v[64:67]
	s_barrier
	s_setprio 0
	s_add_i32 s70, s60, s39
	v_lshl_add_u64 v[210:211], s[30:31], 0, v[148:149]
	s_mov_b32 m0, s70
	ds_read_b128 v[178:181], v165 offset:16384
	ds_read_b128 v[182:185], v165 offset:17408
	ds_read_b128 v[186:189], v165 offset:18432
	ds_read_b128 v[190:193], v165 offset:19456
	ds_read_b128 v[194:197], v165 offset:20480
	ds_read_b128 v[198:201], v165 offset:21504
	ds_read_b128 v[202:205], v165 offset:22528
	ds_read_b128 v[206:209], v165 offset:23552
	global_load_lds_dwordx4 v[210:211], off
	s_add_i32 m0, s70, 0x2000
	s_add_u32 s70, s30, 0x40000
	v_lshl_add_u64 v[212:213], s[30:31], 0, v[144:145]
	s_addc_u32 s71, s31, 0
	s_add_i32 s72, s61, s39
	global_load_lds_dwordx4 v[212:213], off
	v_lshl_add_u64 v[214:215], s[70:71], 0, v[148:149]
	s_mov_b32 m0, s72
	v_lshl_add_u64 v[216:217], s[34:35], 0, v[146:147]
	global_load_lds_dwordx4 v[214:215], off
	v_lshl_add_u64 v[214:215], s[70:71], 0, v[144:145]
	s_add_i32 m0, s72, 0x2000
	s_nop 0
	global_load_lds_dwordx4 v[214:215], off
	v_lshl_add_u64 v[214:215], s[34:35], 0, v[150:151]
	s_mov_b32 m0, s25
	s_nop 0
	global_load_lds_dwordx4 v[214:215], off
	s_mov_b32 m0, s27
	s_nop 0
	global_load_lds_dwordx4 v[216:217], off
	s_waitcnt vmcnt(8)
	s_waitcnt lgkmcnt(0)
	s_setprio 1
	s_barrier
	v_mfma_i32_16x16x64_i8 v[60:63], v[76:79], v[178:181], 0
	v_mfma_i32_16x16x64_i8 v[56:59], v[84:87], v[178:181], 0
	v_mfma_i32_16x16x64_i8 v[44:47], v[76:79], v[186:189], 0
	v_mfma_i32_16x16x64_i8 v[40:43], v[84:87], v[186:189], 0
	v_mfma_i32_16x16x64_i8 v[28:31], v[76:79], v[194:197], 0
	v_mfma_i32_16x16x64_i8 v[24:27], v[84:87], v[194:197], 0
	v_mfma_i32_16x16x64_i8 v[12:15], v[76:79], v[202:205], 0
	v_mfma_i32_16x16x64_i8 v[8:11], v[84:87], v[202:205], 0
	v_mfma_i32_16x16x64_i8 v[60:63], v[80:83], v[182:185], v[60:63]
	v_mfma_i32_16x16x64_i8 v[56:59], v[88:91], v[182:185], v[56:59]
	v_mfma_i32_16x16x64_i8 v[44:47], v[80:83], v[190:193], v[44:47]
	v_mfma_i32_16x16x64_i8 v[40:43], v[88:91], v[190:193], v[40:43]
	v_mfma_i32_16x16x64_i8 v[28:31], v[80:83], v[198:201], v[28:31]
	v_mfma_i32_16x16x64_i8 v[24:27], v[88:91], v[198:201], v[24:27]
	v_mfma_i32_16x16x64_i8 v[12:15], v[80:83], v[206:209], v[12:15]
	v_mfma_i32_16x16x64_i8 v[8:11], v[88:91], v[206:209], v[8:11]
	v_mfma_i32_16x16x64_i8 v[52:55], v[158:161], v[178:181], 0
	v_mfma_i32_16x16x64_i8 v[48:51], v[170:173], v[178:181], 0
	v_mfma_i32_16x16x64_i8 v[36:39], v[158:161], v[186:189], 0
	v_mfma_i32_16x16x64_i8 v[32:35], v[170:173], v[186:189], 0
	v_mfma_i32_16x16x64_i8 v[20:23], v[158:161], v[194:197], 0
	v_mfma_i32_16x16x64_i8 v[16:19], v[170:173], v[194:197], 0
	v_mfma_i32_16x16x64_i8 v[4:7], v[158:161], v[202:205], 0
	v_mfma_i32_16x16x64_i8 v[0:3], v[170:173], v[202:205], 0
	v_mfma_i32_16x16x64_i8 v[52:55], v[166:169], v[182:185], v[52:55]
	v_mfma_i32_16x16x64_i8 v[48:51], v[174:177], v[182:185], v[48:51]
	v_mfma_i32_16x16x64_i8 v[36:39], v[166:169], v[190:193], v[36:39]
	v_mfma_i32_16x16x64_i8 v[32:35], v[174:177], v[190:193], v[32:35]
	v_mfma_i32_16x16x64_i8 v[20:23], v[166:169], v[198:201], v[20:23]
	v_mfma_i32_16x16x64_i8 v[16:19], v[174:177], v[198:201], v[16:19]
	v_mfma_i32_16x16x64_i8 v[4:7], v[166:169], v[206:209], v[4:7]
	v_mfma_i32_16x16x64_i8 v[0:3], v[174:177], v[206:209], v[0:3]
	s_barrier
	s_setprio 0
	s_add_i32 s70, 0, 0x18000
	s_add_i32 s71, 0, 0x1c000
	v_add_u32_e32 v88, s70, v162
	v_add_u32_e32 v174, s71, v162
	ds_read_b128 v[76:79], v88
	ds_read_b128 v[80:83], v88 offset:1024
	ds_read_b128 v[84:87], v88 offset:2048
	ds_read_b128 v[88:91], v88 offset:3072
	ds_read_b128 v[158:161], v174
	ds_read_b128 v[166:169], v174 offset:1024
	ds_read_b128 v[170:173], v174 offset:2048
	ds_read_b128 v[174:177], v174 offset:3072
	s_add_u32 s34, s34, 0x40000
	s_addc_u32 s35, s35, 0
	s_mov_b32 m0, s50
	v_lshl_add_u64 v[218:219], s[34:35], 0, v[150:151]
	ds_read_b128 v[178:181], v165 offset:32768
	ds_read_b128 v[182:185], v165 offset:33792
	ds_read_b128 v[186:189], v165 offset:34816
	ds_read_b128 v[190:193], v165 offset:35840
	ds_read_b128 v[194:197], v165 offset:36864
	ds_read_b128 v[198:201], v165 offset:37888
	ds_read_b128 v[202:205], v165 offset:38912
	ds_read_b128 v[206:209], v165 offset:39936
	global_load_lds_dwordx4 v[218:219], off
	v_lshl_add_u64 v[218:219], s[34:35], 0, v[146:147]
	s_mov_b32 m0, s51
	s_nop 0
	global_load_lds_dwordx4 v[218:219], off
	s_waitcnt vmcnt(8)
	s_waitcnt lgkmcnt(0)
	s_setprio 1
	s_barrier
	v_mfma_i32_16x16x64_i8 v[140:143], v[76:79], v[178:181], v[140:143]
	v_mfma_i32_16x16x64_i8 v[136:139], v[84:87], v[178:181], v[136:139]
	v_mfma_i32_16x16x64_i8 v[124:127], v[76:79], v[186:189], v[124:127]
	v_mfma_i32_16x16x64_i8 v[120:123], v[84:87], v[186:189], v[120:123]
	v_mfma_i32_16x16x64_i8 v[108:111], v[76:79], v[194:197], v[108:111]
	v_mfma_i32_16x16x64_i8 v[104:107], v[84:87], v[194:197], v[104:107]
	v_mfma_i32_16x16x64_i8 v[92:95], v[76:79], v[202:205], v[92:95]
	v_mfma_i32_16x16x64_i8 v[72:75], v[84:87], v[202:205], v[72:75]
	v_mfma_i32_16x16x64_i8 v[140:143], v[80:83], v[182:185], v[140:143]
	v_mfma_i32_16x16x64_i8 v[136:139], v[88:91], v[182:185], v[136:139]
	v_mfma_i32_16x16x64_i8 v[124:127], v[80:83], v[190:193], v[124:127]
	v_mfma_i32_16x16x64_i8 v[120:123], v[88:91], v[190:193], v[120:123]
	v_mfma_i32_16x16x64_i8 v[108:111], v[80:83], v[198:201], v[108:111]
	v_mfma_i32_16x16x64_i8 v[104:107], v[88:91], v[198:201], v[104:107]
	v_mfma_i32_16x16x64_i8 v[92:95], v[80:83], v[206:209], v[92:95]
	v_mfma_i32_16x16x64_i8 v[72:75], v[88:91], v[206:209], v[72:75]
	v_mfma_i32_16x16x64_i8 v[132:135], v[158:161], v[178:181], v[132:135]
	v_mfma_i32_16x16x64_i8 v[128:131], v[170:173], v[178:181], v[128:131]
	v_mfma_i32_16x16x64_i8 v[116:119], v[158:161], v[186:189], v[116:119]
	v_mfma_i32_16x16x64_i8 v[112:115], v[170:173], v[186:189], v[112:115]
	v_mfma_i32_16x16x64_i8 v[100:103], v[158:161], v[194:197], v[100:103]
	v_mfma_i32_16x16x64_i8 v[96:99], v[170:173], v[194:197], v[96:99]
	v_mfma_i32_16x16x64_i8 v[68:71], v[158:161], v[202:205], v[68:71]
	v_mfma_i32_16x16x64_i8 v[64:67], v[170:173], v[202:205], v[64:67]
	v_mfma_i32_16x16x64_i8 v[132:135], v[166:169], v[182:185], v[132:135]
	v_mfma_i32_16x16x64_i8 v[128:131], v[174:177], v[182:185], v[128:131]
	v_mfma_i32_16x16x64_i8 v[116:119], v[166:169], v[190:193], v[116:119]
	v_mfma_i32_16x16x64_i8 v[112:115], v[174:177], v[190:193], v[112:115]
	v_mfma_i32_16x16x64_i8 v[100:103], v[166:169], v[198:201], v[100:103]
	v_mfma_i32_16x16x64_i8 v[96:99], v[174:177], v[198:201], v[96:99]
	v_mfma_i32_16x16x64_i8 v[68:71], v[166:169], v[206:209], v[68:71]
	v_mfma_i32_16x16x64_i8 v[64:67], v[174:177], v[206:209], v[64:67]
	s_barrier
	s_setprio 0
	s_add_i32 s34, s70, s39
	v_lshl_add_u64 v[210:211], v[210:211], 0, s[12:13]
	s_mov_b32 m0, s34
	ds_read_b128 v[178:181], v165 offset:49152
	ds_read_b128 v[182:185], v165 offset:50176
	ds_read_b128 v[186:189], v165 offset:51200
	ds_read_b128 v[190:193], v165 offset:52224
	ds_read_b128 v[194:197], v165 offset:53248
	ds_read_b128 v[198:201], v165 offset:54272
	ds_read_b128 v[202:205], v165 offset:55296
	ds_read_b128 v[206:209], v165 offset:56320
	global_load_lds_dwordx4 v[210:211], off
	s_add_i32 m0, s34, 0x2000
	s_add_u32 s30, s30, 0x40080
	v_lshl_add_u64 v[210:211], v[212:213], 0, s[12:13]
	s_addc_u32 s31, s31, 0
	s_add_i32 s34, s71, s39
	global_load_lds_dwordx4 v[210:211], off
	v_lshl_add_u64 v[210:211], s[30:31], 0, v[148:149]
	s_mov_b32 m0, s34
	s_nop 0
	global_load_lds_dwordx4 v[210:211], off
	v_lshl_add_u64 v[210:211], s[30:31], 0, v[144:145]
	s_add_i32 m0, s34, 0x2000
	s_nop 0
	global_load_lds_dwordx4 v[210:211], off
	v_lshl_add_u64 v[210:211], v[214:215], 0, s[12:13]
	s_mov_b32 m0, s58
	s_nop 0
	global_load_lds_dwordx4 v[210:211], off
	v_lshl_add_u64 v[210:211], v[216:217], 0, s[12:13]
	s_mov_b32 m0, s59
	s_nop 0
	global_load_lds_dwordx4 v[210:211], off
	s_waitcnt vmcnt(8)
	s_waitcnt lgkmcnt(0)
	s_setprio 1
	s_barrier
	v_mfma_i32_16x16x64_i8 v[60:63], v[76:79], v[178:181], v[60:63]
	v_mfma_i32_16x16x64_i8 v[56:59], v[84:87], v[178:181], v[56:59]
	v_mfma_i32_16x16x64_i8 v[44:47], v[76:79], v[186:189], v[44:47]
	v_mfma_i32_16x16x64_i8 v[40:43], v[84:87], v[186:189], v[40:43]
	v_mfma_i32_16x16x64_i8 v[28:31], v[76:79], v[194:197], v[28:31]
	v_mfma_i32_16x16x64_i8 v[24:27], v[84:87], v[194:197], v[24:27]
	v_mfma_i32_16x16x64_i8 v[12:15], v[76:79], v[202:205], v[12:15]
	v_mfma_i32_16x16x64_i8 v[8:11], v[84:87], v[202:205], v[8:11]
	v_mfma_i32_16x16x64_i8 v[60:63], v[80:83], v[182:185], v[60:63]
	v_mfma_i32_16x16x64_i8 v[56:59], v[88:91], v[182:185], v[56:59]
	v_mfma_i32_16x16x64_i8 v[44:47], v[80:83], v[190:193], v[44:47]
	v_mfma_i32_16x16x64_i8 v[40:43], v[88:91], v[190:193], v[40:43]
	v_mfma_i32_16x16x64_i8 v[28:31], v[80:83], v[198:201], v[28:31]
	v_mfma_i32_16x16x64_i8 v[24:27], v[88:91], v[198:201], v[24:27]
	v_mfma_i32_16x16x64_i8 v[12:15], v[80:83], v[206:209], v[12:15]
	v_mfma_i32_16x16x64_i8 v[8:11], v[88:91], v[206:209], v[8:11]
	v_mfma_i32_16x16x64_i8 v[52:55], v[158:161], v[178:181], v[52:55]
	v_mfma_i32_16x16x64_i8 v[48:51], v[170:173], v[178:181], v[48:51]
	v_mfma_i32_16x16x64_i8 v[36:39], v[158:161], v[186:189], v[36:39]
	v_mfma_i32_16x16x64_i8 v[32:35], v[170:173], v[186:189], v[32:35]
	v_mfma_i32_16x16x64_i8 v[20:23], v[158:161], v[194:197], v[20:23]
	v_mfma_i32_16x16x64_i8 v[16:19], v[170:173], v[194:197], v[16:19]
	v_mfma_i32_16x16x64_i8 v[4:7], v[158:161], v[202:205], v[4:7]
	v_mfma_i32_16x16x64_i8 v[0:3], v[170:173], v[202:205], v[0:3]
	v_mfma_i32_16x16x64_i8 v[52:55], v[166:169], v[182:185], v[52:55]
	v_mfma_i32_16x16x64_i8 v[48:51], v[174:177], v[182:185], v[48:51]
	v_mfma_i32_16x16x64_i8 v[36:39], v[166:169], v[190:193], v[36:39]
	v_mfma_i32_16x16x64_i8 v[32:35], v[174:177], v[190:193], v[32:35]
	v_mfma_i32_16x16x64_i8 v[20:23], v[166:169], v[198:201], v[20:23]
	v_mfma_i32_16x16x64_i8 v[16:19], v[174:177], v[198:201], v[16:19]
	v_mfma_i32_16x16x64_i8 v[4:7], v[166:169], v[206:209], v[4:7]
	v_mfma_i32_16x16x64_i8 v[0:3], v[174:177], v[206:209], v[0:3]
	s_barrier
	s_setprio 0
	s_add_i32 s69, s69, 2
	s_add_u32 s28, s28, 0x100
	s_addc_u32 s29, s29, 0
	s_add_u32 s17, s17, 0x100
	s_addc_u32 s19, s19, 0
.LBB0_1848:
	ds_read_b128 v[76:79], v163
	ds_read_b128 v[80:83], v163 offset:1024
	ds_read_b128 v[84:87], v163 offset:2048
	ds_read_b128 v[88:91], v163 offset:3072
	ds_read_b128 v[158:161], v164
	ds_read_b128 v[166:169], v164 offset:1024
	ds_read_b128 v[170:173], v164 offset:2048
	ds_read_b128 v[174:177], v164 offset:3072
	s_add_u32 s30, s28, 0xfffc0080
	s_addc_u32 s31, s29, -1
	s_cmp_eq_u32 s69, 12
	s_cselect_b32 s35, s21, s31
	s_cselect_b32 s34, s20, s30
	s_cselect_b32 s31, s23, s19
	s_cselect_b32 s30, s22, s17
	v_lshl_add_u64 v[210:211], s[28:29], 0, v[152:153]
	s_add_i32 m0, s25, 0xc000
	ds_read_b128 v[178:181], v165
	ds_read_b128 v[182:185], v165 offset:1024
	ds_read_b128 v[186:189], v165 offset:2048
	ds_read_b128 v[190:193], v165 offset:3072
	ds_read_b128 v[194:197], v165 offset:4096
	ds_read_b128 v[198:201], v165 offset:5120
	ds_read_b128 v[202:205], v165 offset:6144
	ds_read_b128 v[206:209], v165 offset:7168
	global_load_lds_dwordx4 v[210:211], off
	v_lshl_add_u64 v[210:211], s[28:29], 0, v[154:155]
	s_add_i32 m0, s25, 0xe000
	s_nop 0
	global_load_lds_dwordx4 v[210:211], off
	s_waitcnt vmcnt(8)
	s_waitcnt lgkmcnt(0)
	s_setprio 1
	s_barrier
	v_mfma_i32_16x16x64_i8 v[140:143], v[76:79], v[178:181], v[140:143]
	v_mfma_i32_16x16x64_i8 v[136:139], v[84:87], v[178:181], v[136:139]
	v_mfma_i32_16x16x64_i8 v[124:127], v[76:79], v[186:189], v[124:127]
	v_mfma_i32_16x16x64_i8 v[120:123], v[84:87], v[186:189], v[120:123]
	v_mfma_i32_16x16x64_i8 v[108:111], v[76:79], v[194:197], v[108:111]
	v_mfma_i32_16x16x64_i8 v[104:107], v[84:87], v[194:197], v[104:107]
	v_mfma_i32_16x16x64_i8 v[92:95], v[76:79], v[202:205], v[92:95]
	v_mfma_i32_16x16x64_i8 v[72:75], v[84:87], v[202:205], v[72:75]
	v_mfma_i32_16x16x64_i8 v[140:143], v[80:83], v[182:185], v[140:143]
	v_mfma_i32_16x16x64_i8 v[136:139], v[88:91], v[182:185], v[136:139]
	v_mfma_i32_16x16x64_i8 v[124:127], v[80:83], v[190:193], v[124:127]
	v_mfma_i32_16x16x64_i8 v[120:123], v[88:91], v[190:193], v[120:123]
	v_mfma_i32_16x16x64_i8 v[108:111], v[80:83], v[198:201], v[108:111]
	v_mfma_i32_16x16x64_i8 v[104:107], v[88:91], v[198:201], v[104:107]
	v_mfma_i32_16x16x64_i8 v[92:95], v[80:83], v[206:209], v[92:95]
	v_mfma_i32_16x16x64_i8 v[72:75], v[88:91], v[206:209], v[72:75]
	v_mfma_i32_16x16x64_i8 v[132:135], v[158:161], v[178:181], v[132:135]
	v_mfma_i32_16x16x64_i8 v[128:131], v[170:173], v[178:181], v[128:131]
	v_mfma_i32_16x16x64_i8 v[116:119], v[158:161], v[186:189], v[116:119]
	v_mfma_i32_16x16x64_i8 v[112:115], v[170:173], v[186:189], v[112:115]
	v_mfma_i32_16x16x64_i8 v[100:103], v[158:161], v[194:197], v[100:103]
	v_mfma_i32_16x16x64_i8 v[96:99], v[170:173], v[194:197], v[96:99]
	v_mfma_i32_16x16x64_i8 v[68:71], v[158:161], v[202:205], v[68:71]
	v_mfma_i32_16x16x64_i8 v[64:67], v[170:173], v[202:205], v[64:67]
	v_mfma_i32_16x16x64_i8 v[132:135], v[166:169], v[182:185], v[132:135]
	v_mfma_i32_16x16x64_i8 v[128:131], v[174:177], v[182:185], v[128:131]
	v_mfma_i32_16x16x64_i8 v[116:119], v[166:169], v[190:193], v[116:119]
	v_mfma_i32_16x16x64_i8 v[112:115], v[174:177], v[190:193], v[112:115]
	v_mfma_i32_16x16x64_i8 v[100:103], v[166:169], v[198:201], v[100:103]
	v_mfma_i32_16x16x64_i8 v[96:99], v[174:177], v[198:201], v[96:99]
	v_mfma_i32_16x16x64_i8 v[68:71], v[166:169], v[206:209], v[68:71]
	v_mfma_i32_16x16x64_i8 v[64:67], v[174:177], v[206:209], v[64:67]
	s_barrier
	s_setprio 0
	s_add_i32 s70, s60, s39
	v_lshl_add_u64 v[210:211], s[30:31], 0, v[148:149]
	s_mov_b32 m0, s70
	ds_read_b128 v[178:181], v165 offset:16384
	ds_read_b128 v[182:185], v165 offset:17408
	ds_read_b128 v[186:189], v165 offset:18432
	ds_read_b128 v[190:193], v165 offset:19456
	ds_read_b128 v[194:197], v165 offset:20480
	ds_read_b128 v[198:201], v165 offset:21504
	ds_read_b128 v[202:205], v165 offset:22528
	ds_read_b128 v[206:209], v165 offset:23552
	global_load_lds_dwordx4 v[210:211], off
	s_add_i32 m0, s70, 0x2000
	s_add_u32 s70, s30, 0x40000
	v_lshl_add_u64 v[212:213], s[30:31], 0, v[144:145]
	s_addc_u32 s71, s31, 0
	s_add_i32 s72, s61, s39
	global_load_lds_dwordx4 v[212:213], off
	v_lshl_add_u64 v[214:215], s[70:71], 0, v[148:149]
	s_mov_b32 m0, s72
	v_lshl_add_u64 v[216:217], s[34:35], 0, v[146:147]
	global_load_lds_dwordx4 v[214:215], off
	v_lshl_add_u64 v[214:215], s[70:71], 0, v[144:145]
	s_add_i32 m0, s72, 0x2000
	s_nop 0
	global_load_lds_dwordx4 v[214:215], off
	v_lshl_add_u64 v[214:215], s[34:35], 0, v[150:151]
	s_mov_b32 m0, s25
	s_nop 0
	global_load_lds_dwordx4 v[214:215], off
	s_mov_b32 m0, s27
	s_nop 0
	global_load_lds_dwordx4 v[216:217], off
	s_waitcnt vmcnt(8)
	s_waitcnt lgkmcnt(0)
	s_setprio 1
	s_barrier
	v_mfma_i32_16x16x64_i8 v[60:63], v[76:79], v[178:181], v[60:63]
	v_mfma_i32_16x16x64_i8 v[56:59], v[84:87], v[178:181], v[56:59]
	v_mfma_i32_16x16x64_i8 v[44:47], v[76:79], v[186:189], v[44:47]
	v_mfma_i32_16x16x64_i8 v[40:43], v[84:87], v[186:189], v[40:43]
	v_mfma_i32_16x16x64_i8 v[28:31], v[76:79], v[194:197], v[28:31]
	v_mfma_i32_16x16x64_i8 v[24:27], v[84:87], v[194:197], v[24:27]
	v_mfma_i32_16x16x64_i8 v[12:15], v[76:79], v[202:205], v[12:15]
	v_mfma_i32_16x16x64_i8 v[8:11], v[84:87], v[202:205], v[8:11]
	v_mfma_i32_16x16x64_i8 v[60:63], v[80:83], v[182:185], v[60:63]
	v_mfma_i32_16x16x64_i8 v[56:59], v[88:91], v[182:185], v[56:59]
	v_mfma_i32_16x16x64_i8 v[44:47], v[80:83], v[190:193], v[44:47]
	v_mfma_i32_16x16x64_i8 v[40:43], v[88:91], v[190:193], v[40:43]
	v_mfma_i32_16x16x64_i8 v[28:31], v[80:83], v[198:201], v[28:31]
	v_mfma_i32_16x16x64_i8 v[24:27], v[88:91], v[198:201], v[24:27]
	v_mfma_i32_16x16x64_i8 v[12:15], v[80:83], v[206:209], v[12:15]
	v_mfma_i32_16x16x64_i8 v[8:11], v[88:91], v[206:209], v[8:11]
	v_mfma_i32_16x16x64_i8 v[52:55], v[158:161], v[178:181], v[52:55]
	v_mfma_i32_16x16x64_i8 v[48:51], v[170:173], v[178:181], v[48:51]
	v_mfma_i32_16x16x64_i8 v[36:39], v[158:161], v[186:189], v[36:39]
	v_mfma_i32_16x16x64_i8 v[32:35], v[170:173], v[186:189], v[32:35]
	v_mfma_i32_16x16x64_i8 v[20:23], v[158:161], v[194:197], v[20:23]
	v_mfma_i32_16x16x64_i8 v[16:19], v[170:173], v[194:197], v[16:19]
	v_mfma_i32_16x16x64_i8 v[4:7], v[158:161], v[202:205], v[4:7]
	v_mfma_i32_16x16x64_i8 v[0:3], v[170:173], v[202:205], v[0:3]
	v_mfma_i32_16x16x64_i8 v[52:55], v[166:169], v[182:185], v[52:55]
	v_mfma_i32_16x16x64_i8 v[48:51], v[174:177], v[182:185], v[48:51]
	v_mfma_i32_16x16x64_i8 v[36:39], v[166:169], v[190:193], v[36:39]
	v_mfma_i32_16x16x64_i8 v[32:35], v[174:177], v[190:193], v[32:35]
	v_mfma_i32_16x16x64_i8 v[20:23], v[166:169], v[198:201], v[20:23]
	v_mfma_i32_16x16x64_i8 v[16:19], v[174:177], v[198:201], v[16:19]
	v_mfma_i32_16x16x64_i8 v[4:7], v[166:169], v[206:209], v[4:7]
	v_mfma_i32_16x16x64_i8 v[0:3], v[174:177], v[206:209], v[0:3]
	s_barrier
	s_setprio 0
	s_add_i32 s70, 0, 0x18000
	s_add_i32 s71, 0, 0x1c000
	v_add_u32_e32 v88, s70, v162
	v_add_u32_e32 v174, s71, v162
	ds_read_b128 v[76:79], v88
	ds_read_b128 v[80:83], v88 offset:1024
	ds_read_b128 v[84:87], v88 offset:2048
	ds_read_b128 v[88:91], v88 offset:3072
	ds_read_b128 v[158:161], v174
	ds_read_b128 v[166:169], v174 offset:1024
	ds_read_b128 v[170:173], v174 offset:2048
	ds_read_b128 v[174:177], v174 offset:3072
	s_add_u32 s34, s34, 0x40000
	s_addc_u32 s35, s35, 0
	s_mov_b32 m0, s50
	v_lshl_add_u64 v[218:219], s[34:35], 0, v[150:151]
	ds_read_b128 v[178:181], v165 offset:32768
	ds_read_b128 v[182:185], v165 offset:33792
	ds_read_b128 v[186:189], v165 offset:34816
	ds_read_b128 v[190:193], v165 offset:35840
	ds_read_b128 v[194:197], v165 offset:36864
	ds_read_b128 v[198:201], v165 offset:37888
	ds_read_b128 v[202:205], v165 offset:38912
	ds_read_b128 v[206:209], v165 offset:39936
	global_load_lds_dwordx4 v[218:219], off
	v_lshl_add_u64 v[218:219], s[34:35], 0, v[146:147]
	s_mov_b32 m0, s51
	s_nop 0
	global_load_lds_dwordx4 v[218:219], off
	s_waitcnt vmcnt(8)
	s_waitcnt lgkmcnt(0)
	s_setprio 1
	s_barrier
	v_mfma_i32_16x16x64_i8 v[140:143], v[76:79], v[178:181], v[140:143]
	v_mfma_i32_16x16x64_i8 v[136:139], v[84:87], v[178:181], v[136:139]
	v_mfma_i32_16x16x64_i8 v[124:127], v[76:79], v[186:189], v[124:127]
	v_mfma_i32_16x16x64_i8 v[120:123], v[84:87], v[186:189], v[120:123]
	v_mfma_i32_16x16x64_i8 v[108:111], v[76:79], v[194:197], v[108:111]
	v_mfma_i32_16x16x64_i8 v[104:107], v[84:87], v[194:197], v[104:107]
	v_mfma_i32_16x16x64_i8 v[92:95], v[76:79], v[202:205], v[92:95]
	v_mfma_i32_16x16x64_i8 v[72:75], v[84:87], v[202:205], v[72:75]
	v_mfma_i32_16x16x64_i8 v[140:143], v[80:83], v[182:185], v[140:143]
	v_mfma_i32_16x16x64_i8 v[136:139], v[88:91], v[182:185], v[136:139]
	v_mfma_i32_16x16x64_i8 v[124:127], v[80:83], v[190:193], v[124:127]
	v_mfma_i32_16x16x64_i8 v[120:123], v[88:91], v[190:193], v[120:123]
	v_mfma_i32_16x16x64_i8 v[108:111], v[80:83], v[198:201], v[108:111]
	v_mfma_i32_16x16x64_i8 v[104:107], v[88:91], v[198:201], v[104:107]
	v_mfma_i32_16x16x64_i8 v[92:95], v[80:83], v[206:209], v[92:95]
	v_mfma_i32_16x16x64_i8 v[72:75], v[88:91], v[206:209], v[72:75]
	v_mfma_i32_16x16x64_i8 v[132:135], v[158:161], v[178:181], v[132:135]
	v_mfma_i32_16x16x64_i8 v[128:131], v[170:173], v[178:181], v[128:131]
	v_mfma_i32_16x16x64_i8 v[116:119], v[158:161], v[186:189], v[116:119]
	v_mfma_i32_16x16x64_i8 v[112:115], v[170:173], v[186:189], v[112:115]
	v_mfma_i32_16x16x64_i8 v[100:103], v[158:161], v[194:197], v[100:103]
	v_mfma_i32_16x16x64_i8 v[96:99], v[170:173], v[194:197], v[96:99]
	v_mfma_i32_16x16x64_i8 v[68:71], v[158:161], v[202:205], v[68:71]
	v_mfma_i32_16x16x64_i8 v[64:67], v[170:173], v[202:205], v[64:67]
	v_mfma_i32_16x16x64_i8 v[132:135], v[166:169], v[182:185], v[132:135]
	v_mfma_i32_16x16x64_i8 v[128:131], v[174:177], v[182:185], v[128:131]
	v_mfma_i32_16x16x64_i8 v[116:119], v[166:169], v[190:193], v[116:119]
	v_mfma_i32_16x16x64_i8 v[112:115], v[174:177], v[190:193], v[112:115]
	v_mfma_i32_16x16x64_i8 v[100:103], v[166:169], v[198:201], v[100:103]
	v_mfma_i32_16x16x64_i8 v[96:99], v[174:177], v[198:201], v[96:99]
	v_mfma_i32_16x16x64_i8 v[68:71], v[166:169], v[206:209], v[68:71]
	v_mfma_i32_16x16x64_i8 v[64:67], v[174:177], v[206:209], v[64:67]
	s_barrier
	s_setprio 0
	s_add_i32 s34, s70, s39
	v_lshl_add_u64 v[210:211], v[210:211], 0, s[12:13]
	s_mov_b32 m0, s34
	ds_read_b128 v[178:181], v165 offset:49152
	ds_read_b128 v[182:185], v165 offset:50176
	ds_read_b128 v[186:189], v165 offset:51200
	ds_read_b128 v[190:193], v165 offset:52224
	ds_read_b128 v[194:197], v165 offset:53248
	ds_read_b128 v[198:201], v165 offset:54272
	ds_read_b128 v[202:205], v165 offset:55296
	ds_read_b128 v[206:209], v165 offset:56320
	global_load_lds_dwordx4 v[210:211], off
	s_add_i32 m0, s34, 0x2000
	s_add_u32 s30, s30, 0x40080
	v_lshl_add_u64 v[210:211], v[212:213], 0, s[12:13]
	s_addc_u32 s31, s31, 0
	s_add_i32 s34, s71, s39
	global_load_lds_dwordx4 v[210:211], off
	v_lshl_add_u64 v[210:211], s[30:31], 0, v[148:149]
	s_mov_b32 m0, s34
	s_nop 0
	global_load_lds_dwordx4 v[210:211], off
	v_lshl_add_u64 v[210:211], s[30:31], 0, v[144:145]
	s_add_i32 m0, s34, 0x2000
	s_nop 0
	global_load_lds_dwordx4 v[210:211], off
	v_lshl_add_u64 v[210:211], v[214:215], 0, s[12:13]
	s_mov_b32 m0, s58
	s_nop 0
	global_load_lds_dwordx4 v[210:211], off
	v_lshl_add_u64 v[210:211], v[216:217], 0, s[12:13]
	s_mov_b32 m0, s59
	s_nop 0
	global_load_lds_dwordx4 v[210:211], off
	s_waitcnt vmcnt(8)
	s_waitcnt lgkmcnt(0)
	s_setprio 1
	s_barrier
	v_mfma_i32_16x16x64_i8 v[60:63], v[76:79], v[178:181], v[60:63]
	v_mfma_i32_16x16x64_i8 v[56:59], v[84:87], v[178:181], v[56:59]
	v_mfma_i32_16x16x64_i8 v[44:47], v[76:79], v[186:189], v[44:47]
	v_mfma_i32_16x16x64_i8 v[40:43], v[84:87], v[186:189], v[40:43]
	v_mfma_i32_16x16x64_i8 v[28:31], v[76:79], v[194:197], v[28:31]
	v_mfma_i32_16x16x64_i8 v[24:27], v[84:87], v[194:197], v[24:27]
	v_mfma_i32_16x16x64_i8 v[12:15], v[76:79], v[202:205], v[12:15]
	v_mfma_i32_16x16x64_i8 v[8:11], v[84:87], v[202:205], v[8:11]
	v_mfma_i32_16x16x64_i8 v[60:63], v[80:83], v[182:185], v[60:63]
	v_mfma_i32_16x16x64_i8 v[56:59], v[88:91], v[182:185], v[56:59]
	v_mfma_i32_16x16x64_i8 v[44:47], v[80:83], v[190:193], v[44:47]
	v_mfma_i32_16x16x64_i8 v[40:43], v[88:91], v[190:193], v[40:43]
	v_mfma_i32_16x16x64_i8 v[28:31], v[80:83], v[198:201], v[28:31]
	v_mfma_i32_16x16x64_i8 v[24:27], v[88:91], v[198:201], v[24:27]
	v_mfma_i32_16x16x64_i8 v[12:15], v[80:83], v[206:209], v[12:15]
	v_mfma_i32_16x16x64_i8 v[8:11], v[88:91], v[206:209], v[8:11]
	v_mfma_i32_16x16x64_i8 v[52:55], v[158:161], v[178:181], v[52:55]
	v_mfma_i32_16x16x64_i8 v[48:51], v[170:173], v[178:181], v[48:51]
	v_mfma_i32_16x16x64_i8 v[36:39], v[158:161], v[186:189], v[36:39]
	v_mfma_i32_16x16x64_i8 v[32:35], v[170:173], v[186:189], v[32:35]
	v_mfma_i32_16x16x64_i8 v[20:23], v[158:161], v[194:197], v[20:23]
	v_mfma_i32_16x16x64_i8 v[16:19], v[170:173], v[194:197], v[16:19]
	v_mfma_i32_16x16x64_i8 v[4:7], v[158:161], v[202:205], v[4:7]
	v_mfma_i32_16x16x64_i8 v[0:3], v[170:173], v[202:205], v[0:3]
	v_mfma_i32_16x16x64_i8 v[52:55], v[166:169], v[182:185], v[52:55]
	v_mfma_i32_16x16x64_i8 v[48:51], v[174:177], v[182:185], v[48:51]
	v_mfma_i32_16x16x64_i8 v[36:39], v[166:169], v[190:193], v[36:39]
	v_mfma_i32_16x16x64_i8 v[32:35], v[174:177], v[190:193], v[32:35]
	v_mfma_i32_16x16x64_i8 v[20:23], v[166:169], v[198:201], v[20:23]
	v_mfma_i32_16x16x64_i8 v[16:19], v[174:177], v[198:201], v[16:19]
	v_mfma_i32_16x16x64_i8 v[4:7], v[166:169], v[206:209], v[4:7]
	v_mfma_i32_16x16x64_i8 v[0:3], v[174:177], v[206:209], v[0:3]
	s_barrier
	s_setprio 0
	s_add_i32 s69, s69, 2
	s_add_u32 s28, s28, 0x100
	s_addc_u32 s29, s29, 0
	s_add_u32 s17, s17, 0x100
	s_addc_u32 s19, s19, 0
	s_cmp_gt_u32 s69, 13
	s_cbranch_scc0 .LBB0_1848

.LBB0_1923:
	ds_read_b128 v[144:147], v137
	ds_read_b128 v[148:151], v137 offset:1024
	ds_read_b128 v[152:155], v137 offset:2048
	ds_read_b128 v[156:159], v137 offset:3072
	ds_read_b128 v[160:163], v138
	ds_read_b128 v[164:167], v138 offset:1024
	ds_read_b128 v[168:171], v138 offset:2048
	ds_read_b128 v[172:175], v138 offset:3072
	s_add_u32 s26, s24, 0x100
	s_addc_u32 s27, s25, 0
	s_cmp_eq_u32 s85, 52
	s_cselect_b32 s34, s18, s26
	s_cselect_b32 s35, s19, s27
	s_cselect_b32 s30, s20, s23
	s_cselect_b32 s31, s21, s84
	s_add_u32 s28, s34, 0x80
	s_addc_u32 s29, s35, 0
	ds_read_b128 v[176:179], v139
	ds_read_b128 v[180:183], v139 offset:1024
	ds_read_b128 v[184:187], v139 offset:2048
	ds_read_b128 v[188:191], v139 offset:3072
	ds_read_b128 v[192:195], v139 offset:4096
	ds_read_b128 v[196:199], v139 offset:5120
	ds_read_b128 v[200:203], v139 offset:6144
	ds_read_b128 v[204:207], v139 offset:7168
	s_add_u32 s24, s24, 0xe0080
	s_addc_u32 s25, s25, 0
	s_mov_b32 s86, m0
	s_mov_b32 m0, s73
	s_nop 0
	global_load_lds_dwordx4 v128, s[24:25]
	s_mov_b32 m0, s86
	s_nop 0
	s_mov_b32 s86, m0
	s_mov_b32 m0, s74
	s_nop 0
	global_load_lds_dwordx4 v130, s[24:25]
	s_mov_b32 m0, s86
	s_waitcnt vmcnt(8)
	s_waitcnt lgkmcnt(0)
	s_setprio 1
	s_barrier
	v_mfma_f32_16x16x128_f8f6f4 v[124:127], v[144:151], v[176:183], v[124:127]
	v_mfma_f32_16x16x128_f8f6f4 v[120:123], v[152:159], v[176:183], v[120:123]
	v_mfma_f32_16x16x128_f8f6f4 v[116:119], v[144:151], v[184:191], v[116:119]
	v_mfma_f32_16x16x128_f8f6f4 v[112:115], v[152:159], v[184:191], v[112:115]
	v_mfma_f32_16x16x128_f8f6f4 v[108:111], v[144:151], v[192:199], v[108:111]
	v_mfma_f32_16x16x128_f8f6f4 v[100:103], v[152:159], v[192:199], v[100:103]
	v_mfma_f32_16x16x128_f8f6f4 v[208:211], v[144:151], v[200:207], v[92:95]
	v_mfma_f32_16x16x128_f8f6f4 v[212:215], v[152:159], v[200:207], v[72:75]
	v_mfma_f32_16x16x128_f8f6f4 v[104:107], v[160:167], v[176:183], v[104:107]
	v_mfma_f32_16x16x128_f8f6f4 v[96:99], v[168:175], v[176:183], v[96:99]
	v_mfma_f32_16x16x128_f8f6f4 v[176:179], v[160:167], v[184:191], v[88:91]
	v_mfma_f32_16x16x128_f8f6f4 v[180:183], v[168:175], v[184:191], v[84:87]
	v_mfma_f32_16x16x128_f8f6f4 v[184:187], v[160:167], v[192:199], v[80:83]
	v_mfma_f32_16x16x128_f8f6f4 v[188:191], v[168:175], v[192:199], v[76:79]
	v_mfma_f32_16x16x128_f8f6f4 v[192:195], v[160:167], v[200:207], v[68:71]
	v_mfma_f32_16x16x128_f8f6f4 v[196:199], v[168:175], v[200:207], v[64:67]
	s_barrier
	s_setprio 0
	s_nop 4
	ds_read_b128 v[64:67], v139 offset:16384
	ds_read_b128 v[68:71], v139 offset:17408
	ds_read_b128 v[72:75], v139 offset:18432
	ds_read_b128 v[76:79], v139 offset:19456
	ds_read_b128 v[80:83], v139 offset:20480
	ds_read_b128 v[84:87], v139 offset:21504
	ds_read_b128 v[88:91], v139 offset:22528
	ds_read_b128 v[92:95], v139 offset:23552
	s_mov_b32 s24, m0
	s_mov_b32 m0, s52
	s_nop 0
	global_load_lds_dwordx4 v129, s[30:31]
	s_mov_b32 m0, s24
	s_nop 0
	s_mov_b32 s24, m0
	s_mov_b32 m0, s53
	s_nop 0
	global_load_lds_dwordx4 v131, s[30:31]
	s_mov_b32 m0, s24
	s_add_u32 s24, s30, 0xe0000
	s_addc_u32 s25, s31, 0
	s_mov_b32 s86, m0
	s_mov_b32 m0, s54
	s_nop 0
	global_load_lds_dwordx4 v129, s[24:25]
	s_mov_b32 m0, s86
	s_nop 0
	s_mov_b32 s86, m0
	s_mov_b32 m0, s55
	s_nop 0
	global_load_lds_dwordx4 v131, s[24:25]
	s_mov_b32 m0, s86
	s_mov_b32 s24, m0
	s_mov_b32 m0, s37
	s_nop 0
	global_load_lds_dwordx4 v128, s[34:35]
	s_mov_b32 m0, s24
	s_nop 0
	s_mov_b32 s24, m0
	s_mov_b32 m0, s56
	s_nop 0
	global_load_lds_dwordx4 v130, s[34:35]
	s_mov_b32 m0, s24
	s_waitcnt vmcnt(8)
	s_waitcnt lgkmcnt(0)
	s_setprio 1
	s_barrier
	v_mfma_f32_16x16x128_f8f6f4 v[60:63], v[144:151], v[64:71], v[60:63]
	v_mfma_f32_16x16x128_f8f6f4 v[56:59], v[152:159], v[64:71], v[56:59]
	v_mfma_f32_16x16x128_f8f6f4 v[48:51], v[144:151], v[72:79], v[48:51]
	v_mfma_f32_16x16x128_f8f6f4 v[200:203], v[152:159], v[72:79], v[40:43]
	v_mfma_f32_16x16x128_f8f6f4 v[204:207], v[144:151], v[80:87], v[32:35]
	v_mfma_f32_16x16x128_f8f6f4 v[216:219], v[152:159], v[80:87], v[24:27]
	v_mfma_f32_16x16x128_f8f6f4 v[220:223], v[144:151], v[88:95], v[16:19]
	v_mfma_f32_16x16x128_f8f6f4 v[224:227], v[152:159], v[88:95], v[8:11]
	v_mfma_f32_16x16x128_f8f6f4 v[52:55], v[160:167], v[64:71], v[52:55]
	v_mfma_f32_16x16x128_f8f6f4 v[228:231], v[168:175], v[64:71], v[44:47]
	v_mfma_f32_16x16x128_f8f6f4 v[232:235], v[160:167], v[72:79], v[36:39]
	v_mfma_f32_16x16x128_f8f6f4 v[236:239], v[168:175], v[72:79], v[28:31]
	v_mfma_f32_16x16x128_f8f6f4 v[240:243], v[160:167], v[80:87], v[20:23]
	v_mfma_f32_16x16x128_f8f6f4 v[244:247], v[168:175], v[80:87], v[12:15]
	v_mfma_f32_16x16x128_f8f6f4 v[248:251], v[160:167], v[88:95], v[4:7]
	v_mfma_f32_16x16x128_f8f6f4 v[132:135], v[168:175], v[88:95], v[0:3]
	s_barrier
	s_setprio 0
	s_nop 4
	ds_read_b128 v[0:3], v140
	ds_read_b128 v[4:7], v140 offset:1024
	ds_read_b128 v[8:11], v140 offset:2048
	ds_read_b128 v[12:15], v140 offset:3072
	ds_read_b128 v[144:147], v141
	ds_read_b128 v[148:151], v141 offset:1024
	ds_read_b128 v[152:155], v141 offset:2048
	ds_read_b128 v[156:159], v141 offset:3072
	ds_read_b128 v[16:19], v139 offset:32768
	ds_read_b128 v[20:23], v139 offset:33792
	ds_read_b128 v[24:27], v139 offset:34816
	ds_read_b128 v[28:31], v139 offset:35840
	ds_read_b128 v[32:35], v139 offset:36864
	ds_read_b128 v[36:39], v139 offset:37888
	ds_read_b128 v[40:43], v139 offset:38912
	ds_read_b128 v[44:47], v139 offset:39936
	s_add_u32 s24, s34, 0xe0000
	s_addc_u32 s25, s35, 0
	s_mov_b32 s34, m0
	s_mov_b32 m0, s57
	s_nop 0
	global_load_lds_dwordx4 v128, s[24:25]
	s_mov_b32 m0, s34
	s_nop 0
	s_mov_b32 s34, m0
	s_mov_b32 m0, s58
	s_nop 0
	global_load_lds_dwordx4 v130, s[24:25]
	s_mov_b32 m0, s34
	s_waitcnt vmcnt(8)
	s_waitcnt lgkmcnt(0)
	s_setprio 1
	s_barrier
	v_mfma_f32_16x16x128_f8f6f4 v[124:127], v[0:7], v[16:23], v[124:127]
	v_mfma_f32_16x16x128_f8f6f4 v[120:123], v[8:15], v[16:23], v[120:123]
	v_mfma_f32_16x16x128_f8f6f4 v[116:119], v[0:7], v[24:31], v[116:119]
	v_mfma_f32_16x16x128_f8f6f4 v[112:115], v[8:15], v[24:31], v[112:115]
	v_mfma_f32_16x16x128_f8f6f4 v[108:111], v[0:7], v[32:39], v[108:111]
	v_mfma_f32_16x16x128_f8f6f4 v[100:103], v[8:15], v[32:39], v[100:103]
	v_mfma_f32_16x16x128_f8f6f4 v[92:95], v[0:7], v[40:47], v[208:211]
	v_mfma_f32_16x16x128_f8f6f4 v[72:75], v[8:15], v[40:47], v[212:215]
	v_mfma_f32_16x16x128_f8f6f4 v[104:107], v[144:151], v[16:23], v[104:107]
	v_mfma_f32_16x16x128_f8f6f4 v[96:99], v[152:159], v[16:23], v[96:99]
	v_mfma_f32_16x16x128_f8f6f4 v[88:91], v[144:151], v[24:31], v[176:179]
	v_mfma_f32_16x16x128_f8f6f4 v[84:87], v[152:159], v[24:31], v[180:183]
	v_mfma_f32_16x16x128_f8f6f4 v[80:83], v[144:151], v[32:39], v[184:187]
	v_mfma_f32_16x16x128_f8f6f4 v[76:79], v[152:159], v[32:39], v[188:191]
	v_mfma_f32_16x16x128_f8f6f4 v[68:71], v[144:151], v[40:47], v[192:195]
	v_mfma_f32_16x16x128_f8f6f4 v[64:67], v[152:159], v[40:47], v[196:199]
	s_barrier
	s_setprio 0
	ds_read_b128 v[160:163], v139 offset:49152
	ds_read_b128 v[164:167], v139 offset:50176
	ds_read_b128 v[168:171], v139 offset:51200
	ds_read_b128 v[172:175], v139 offset:52224
	ds_read_b128 v[176:179], v139 offset:53248
	ds_read_b128 v[180:183], v139 offset:54272
	ds_read_b128 v[184:187], v139 offset:55296
	ds_read_b128 v[188:191], v139 offset:56320
	s_add_u32 s24, s30, 0x80
	s_addc_u32 s25, s31, 0
	s_mov_b32 s34, m0
	s_mov_b32 m0, s63
	s_nop 0
	global_load_lds_dwordx4 v129, s[24:25]
	s_mov_b32 m0, s34
	s_nop 0
	s_mov_b32 s34, m0
	s_mov_b32 m0, s68
	s_nop 0
	global_load_lds_dwordx4 v131, s[24:25]
	s_mov_b32 m0, s34
	s_add_u32 s24, s30, 0xe0080
	s_addc_u32 s25, s31, 0
	s_mov_b32 s30, m0
	s_mov_b32 m0, s71
	s_nop 0
	global_load_lds_dwordx4 v129, s[24:25]
	s_mov_b32 m0, s30
	s_nop 0
	s_mov_b32 s30, m0
	s_mov_b32 m0, s72
	s_nop 0
	global_load_lds_dwordx4 v131, s[24:25]
	s_mov_b32 m0, s30
	s_mov_b32 s24, m0
	s_mov_b32 m0, s69
	s_nop 0
	global_load_lds_dwordx4 v128, s[28:29]
	s_mov_b32 m0, s24
	s_nop 0
	s_mov_b32 s24, m0
	s_mov_b32 m0, s70
	s_nop 0
	global_load_lds_dwordx4 v130, s[28:29]
	s_mov_b32 m0, s24
	s_waitcnt vmcnt(8)
	s_waitcnt lgkmcnt(0)
	s_setprio 1
	s_barrier
	v_mfma_f32_16x16x128_f8f6f4 v[60:63], v[0:7], v[160:167], v[60:63]
	v_mfma_f32_16x16x128_f8f6f4 v[56:59], v[8:15], v[160:167], v[56:59]
	v_mfma_f32_16x16x128_f8f6f4 v[48:51], v[0:7], v[168:175], v[48:51]
	v_mfma_f32_16x16x128_f8f6f4 v[40:43], v[8:15], v[168:175], v[200:203]
	v_mfma_f32_16x16x128_f8f6f4 v[32:35], v[0:7], v[176:183], v[204:207]
	v_mfma_f32_16x16x128_f8f6f4 v[24:27], v[8:15], v[176:183], v[216:219]
	v_mfma_f32_16x16x128_f8f6f4 v[16:19], v[0:7], v[184:191], v[220:223]
	v_mfma_f32_16x16x128_f8f6f4 v[8:11], v[8:15], v[184:191], v[224:227]
	v_mfma_f32_16x16x128_f8f6f4 v[52:55], v[144:151], v[160:167], v[52:55]
	v_mfma_f32_16x16x128_f8f6f4 v[44:47], v[152:159], v[160:167], v[228:231]
	v_mfma_f32_16x16x128_f8f6f4 v[36:39], v[144:151], v[168:175], v[232:235]
	v_mfma_f32_16x16x128_f8f6f4 v[28:31], v[152:159], v[168:175], v[236:239]
	v_mfma_f32_16x16x128_f8f6f4 v[20:23], v[144:151], v[176:183], v[240:243]
	v_mfma_f32_16x16x128_f8f6f4 v[12:15], v[152:159], v[176:183], v[244:247]
	v_mfma_f32_16x16x128_f8f6f4 v[4:7], v[144:151], v[184:191], v[248:251]
	v_mfma_f32_16x16x128_f8f6f4 v[0:3], v[152:159], v[184:191], v[132:135]
	s_barrier
	s_setprio 0
	s_add_i32 s85, s85, 2
	s_add_u32 s23, s23, 0x100
	s_addc_u32 s84, s84, 0
	s_cmp_gt_u32 s85, 53
	s_mov_b64 s[24:25], s[26:27]
	s_cbranch_scc0 .LBB0_1923
	s_and_b64 vcc, exec, s[8:9]
	s_cbranch_vccz .LBB0_1926
	s_barrier

.LBB0_2007:
	ds_read_b128 v[144:147], v137
	ds_read_b128 v[148:151], v137 offset:1024
	ds_read_b128 v[152:155], v137 offset:2048
	ds_read_b128 v[156:159], v137 offset:3072
	ds_read_b128 v[160:163], v138
	ds_read_b128 v[164:167], v138 offset:1024
	ds_read_b128 v[168:171], v138 offset:2048
	ds_read_b128 v[172:175], v138 offset:3072
	s_add_u32 s26, s24, 0x100
	s_addc_u32 s27, s25, 0
	s_cmp_eq_u32 s86, 52
	s_cselect_b32 s34, s18, s26
	s_cselect_b32 s35, s19, s27
	s_cselect_b32 s30, s20, s23
	s_cselect_b32 s31, s21, s85
	s_add_u32 s28, s34, 0x80
	s_addc_u32 s29, s35, 0
	ds_read_b128 v[176:179], v139
	ds_read_b128 v[180:183], v139 offset:1024
	ds_read_b128 v[184:187], v139 offset:2048
	ds_read_b128 v[188:191], v139 offset:3072
	ds_read_b128 v[192:195], v139 offset:4096
	ds_read_b128 v[196:199], v139 offset:5120
	ds_read_b128 v[200:203], v139 offset:6144
	ds_read_b128 v[204:207], v139 offset:7168
	s_add_u32 s24, s24, 0xe0080
	s_addc_u32 s25, s25, 0
	s_mov_b32 s88, m0
	s_mov_b32 m0, s74
	s_nop 0
	global_load_lds_dwordx4 v128, s[24:25]
	s_mov_b32 m0, s88
	s_nop 0
	s_mov_b32 s88, m0
	s_mov_b32 m0, s75
	s_nop 0
	global_load_lds_dwordx4 v130, s[24:25]
	s_mov_b32 m0, s88
	s_waitcnt vmcnt(8)
	s_waitcnt lgkmcnt(0)
	s_setprio 1
	s_barrier
	v_mfma_f32_16x16x128_f8f6f4 v[124:127], v[144:151], v[176:183], v[124:127]
	v_mfma_f32_16x16x128_f8f6f4 v[120:123], v[152:159], v[176:183], v[120:123]
	v_mfma_f32_16x16x128_f8f6f4 v[116:119], v[144:151], v[184:191], v[116:119]
	v_mfma_f32_16x16x128_f8f6f4 v[112:115], v[152:159], v[184:191], v[112:115]
	v_mfma_f32_16x16x128_f8f6f4 v[108:111], v[144:151], v[192:199], v[108:111]
	v_mfma_f32_16x16x128_f8f6f4 v[100:103], v[152:159], v[192:199], v[100:103]
	v_mfma_f32_16x16x128_f8f6f4 v[208:211], v[144:151], v[200:207], v[92:95]
	v_mfma_f32_16x16x128_f8f6f4 v[212:215], v[152:159], v[200:207], v[72:75]
	v_mfma_f32_16x16x128_f8f6f4 v[104:107], v[160:167], v[176:183], v[104:107]
	v_mfma_f32_16x16x128_f8f6f4 v[96:99], v[168:175], v[176:183], v[96:99]
	v_mfma_f32_16x16x128_f8f6f4 v[176:179], v[160:167], v[184:191], v[88:91]
	v_mfma_f32_16x16x128_f8f6f4 v[180:183], v[168:175], v[184:191], v[84:87]
	v_mfma_f32_16x16x128_f8f6f4 v[184:187], v[160:167], v[192:199], v[80:83]
	v_mfma_f32_16x16x128_f8f6f4 v[188:191], v[168:175], v[192:199], v[76:79]
	v_mfma_f32_16x16x128_f8f6f4 v[192:195], v[160:167], v[200:207], v[68:71]
	v_mfma_f32_16x16x128_f8f6f4 v[196:199], v[168:175], v[200:207], v[64:67]
	s_barrier
	s_setprio 0
	s_nop 4
	ds_read_b128 v[64:67], v139 offset:16384
	ds_read_b128 v[68:71], v139 offset:17408
	ds_read_b128 v[72:75], v139 offset:18432
	ds_read_b128 v[76:79], v139 offset:19456
	ds_read_b128 v[80:83], v139 offset:20480
	ds_read_b128 v[84:87], v139 offset:21504
	ds_read_b128 v[88:91], v139 offset:22528
	ds_read_b128 v[92:95], v139 offset:23552
	s_mov_b32 s24, m0
	s_mov_b32 m0, s53
	s_nop 0
	global_load_lds_dwordx4 v129, s[30:31]
	s_mov_b32 m0, s24
	s_nop 0
	s_mov_b32 s24, m0
	s_mov_b32 m0, s54
	s_nop 0
	global_load_lds_dwordx4 v131, s[30:31]
	s_mov_b32 m0, s24
	s_add_u32 s24, s30, 0xe0000
	s_addc_u32 s25, s31, 0
	s_mov_b32 s88, m0
	s_mov_b32 m0, s55
	s_nop 0
	global_load_lds_dwordx4 v129, s[24:25]
	s_mov_b32 m0, s88
	s_nop 0
	s_mov_b32 s88, m0
	s_mov_b32 m0, s56
	s_nop 0
	global_load_lds_dwordx4 v131, s[24:25]
	s_mov_b32 m0, s88
	s_mov_b32 s24, m0
	s_mov_b32 m0, s43
	s_nop 0
	global_load_lds_dwordx4 v128, s[34:35]
	s_mov_b32 m0, s24
	s_nop 0
	s_mov_b32 s24, m0
	s_mov_b32 m0, s57
	s_nop 0
	global_load_lds_dwordx4 v130, s[34:35]
	s_mov_b32 m0, s24
	s_waitcnt vmcnt(8)
	s_waitcnt lgkmcnt(0)
	s_setprio 1
	s_barrier
	v_mfma_f32_16x16x128_f8f6f4 v[60:63], v[144:151], v[64:71], v[60:63]
	v_mfma_f32_16x16x128_f8f6f4 v[56:59], v[152:159], v[64:71], v[56:59]
	v_mfma_f32_16x16x128_f8f6f4 v[48:51], v[144:151], v[72:79], v[48:51]
	v_mfma_f32_16x16x128_f8f6f4 v[200:203], v[152:159], v[72:79], v[40:43]
	v_mfma_f32_16x16x128_f8f6f4 v[204:207], v[144:151], v[80:87], v[32:35]
	v_mfma_f32_16x16x128_f8f6f4 v[216:219], v[152:159], v[80:87], v[24:27]
	v_mfma_f32_16x16x128_f8f6f4 v[220:223], v[144:151], v[88:95], v[16:19]
	v_mfma_f32_16x16x128_f8f6f4 v[224:227], v[152:159], v[88:95], v[8:11]
	v_mfma_f32_16x16x128_f8f6f4 v[52:55], v[160:167], v[64:71], v[52:55]
	v_mfma_f32_16x16x128_f8f6f4 v[228:231], v[168:175], v[64:71], v[44:47]
	v_mfma_f32_16x16x128_f8f6f4 v[232:235], v[160:167], v[72:79], v[36:39]
	v_mfma_f32_16x16x128_f8f6f4 v[236:239], v[168:175], v[72:79], v[28:31]
	v_mfma_f32_16x16x128_f8f6f4 v[240:243], v[160:167], v[80:87], v[20:23]
	v_mfma_f32_16x16x128_f8f6f4 v[244:247], v[168:175], v[80:87], v[12:15]
	v_mfma_f32_16x16x128_f8f6f4 v[248:251], v[160:167], v[88:95], v[4:7]
	v_mfma_f32_16x16x128_f8f6f4 v[132:135], v[168:175], v[88:95], v[0:3]
	s_barrier
	s_setprio 0
	s_nop 4
	ds_read_b128 v[0:3], v140
	ds_read_b128 v[4:7], v140 offset:1024
	ds_read_b128 v[8:11], v140 offset:2048
	ds_read_b128 v[12:15], v140 offset:3072
	ds_read_b128 v[144:147], v141
	ds_read_b128 v[148:151], v141 offset:1024
	ds_read_b128 v[152:155], v141 offset:2048
	ds_read_b128 v[156:159], v141 offset:3072
	ds_read_b128 v[16:19], v139 offset:32768
	ds_read_b128 v[20:23], v139 offset:33792
	ds_read_b128 v[24:27], v139 offset:34816
	ds_read_b128 v[28:31], v139 offset:35840
	ds_read_b128 v[32:35], v139 offset:36864
	ds_read_b128 v[36:39], v139 offset:37888
	ds_read_b128 v[40:43], v139 offset:38912
	ds_read_b128 v[44:47], v139 offset:39936
	s_add_u32 s24, s34, 0xe0000
	s_addc_u32 s25, s35, 0
	s_mov_b32 s34, m0
	s_mov_b32 m0, s58
	s_nop 0
	global_load_lds_dwordx4 v128, s[24:25]
	s_mov_b32 m0, s34
	s_nop 0
	s_mov_b32 s34, m0
	s_mov_b32 m0, s59
	s_nop 0
	global_load_lds_dwordx4 v130, s[24:25]
	s_mov_b32 m0, s34
	s_waitcnt vmcnt(8)
	s_waitcnt lgkmcnt(0)
	s_setprio 1
	s_barrier
	v_mfma_f32_16x16x128_f8f6f4 v[124:127], v[0:7], v[16:23], v[124:127]
	v_mfma_f32_16x16x128_f8f6f4 v[120:123], v[8:15], v[16:23], v[120:123]
	v_mfma_f32_16x16x128_f8f6f4 v[116:119], v[0:7], v[24:31], v[116:119]
	v_mfma_f32_16x16x128_f8f6f4 v[112:115], v[8:15], v[24:31], v[112:115]
	v_mfma_f32_16x16x128_f8f6f4 v[108:111], v[0:7], v[32:39], v[108:111]
	v_mfma_f32_16x16x128_f8f6f4 v[100:103], v[8:15], v[32:39], v[100:103]
	v_mfma_f32_16x16x128_f8f6f4 v[92:95], v[0:7], v[40:47], v[208:211]
	v_mfma_f32_16x16x128_f8f6f4 v[72:75], v[8:15], v[40:47], v[212:215]
	v_mfma_f32_16x16x128_f8f6f4 v[104:107], v[144:151], v[16:23], v[104:107]
	v_mfma_f32_16x16x128_f8f6f4 v[96:99], v[152:159], v[16:23], v[96:99]
	v_mfma_f32_16x16x128_f8f6f4 v[88:91], v[144:151], v[24:31], v[176:179]
	v_mfma_f32_16x16x128_f8f6f4 v[84:87], v[152:159], v[24:31], v[180:183]
	v_mfma_f32_16x16x128_f8f6f4 v[80:83], v[144:151], v[32:39], v[184:187]
	v_mfma_f32_16x16x128_f8f6f4 v[76:79], v[152:159], v[32:39], v[188:191]
	v_mfma_f32_16x16x128_f8f6f4 v[68:71], v[144:151], v[40:47], v[192:195]
	v_mfma_f32_16x16x128_f8f6f4 v[64:67], v[152:159], v[40:47], v[196:199]
	s_barrier
	s_setprio 0
	ds_read_b128 v[160:163], v139 offset:49152
	ds_read_b128 v[164:167], v139 offset:50176
	ds_read_b128 v[168:171], v139 offset:51200
	ds_read_b128 v[172:175], v139 offset:52224
	ds_read_b128 v[176:179], v139 offset:53248
	ds_read_b128 v[180:183], v139 offset:54272
	ds_read_b128 v[184:187], v139 offset:55296
	ds_read_b128 v[188:191], v139 offset:56320
	s_add_u32 s24, s30, 0x80
	s_addc_u32 s25, s31, 0
	s_mov_b32 s34, m0
	s_mov_b32 m0, s68
	s_nop 0
	global_load_lds_dwordx4 v129, s[24:25]
	s_mov_b32 m0, s34
	s_nop 0
	s_mov_b32 s34, m0
	s_mov_b32 m0, s69
	s_nop 0
	global_load_lds_dwordx4 v131, s[24:25]
	s_mov_b32 m0, s34
	s_add_u32 s24, s30, 0xe0080
	s_addc_u32 s25, s31, 0
	s_mov_b32 s30, m0
	s_mov_b32 m0, s72
	s_nop 0
	global_load_lds_dwordx4 v129, s[24:25]
	s_mov_b32 m0, s30
	s_nop 0
	s_mov_b32 s30, m0
	s_mov_b32 m0, s73
	s_nop 0
	global_load_lds_dwordx4 v131, s[24:25]
	s_mov_b32 m0, s30
	s_mov_b32 s24, m0
	s_mov_b32 m0, s70
	s_nop 0
	global_load_lds_dwordx4 v128, s[28:29]
	s_mov_b32 m0, s24
	s_nop 0
	s_mov_b32 s24, m0
	s_mov_b32 m0, s71
	s_nop 0
	global_load_lds_dwordx4 v130, s[28:29]
	s_mov_b32 m0, s24
	s_waitcnt vmcnt(8)
	s_waitcnt lgkmcnt(0)
	s_setprio 1
	s_barrier
	v_mfma_f32_16x16x128_f8f6f4 v[60:63], v[0:7], v[160:167], v[60:63]
	v_mfma_f32_16x16x128_f8f6f4 v[56:59], v[8:15], v[160:167], v[56:59]
	v_mfma_f32_16x16x128_f8f6f4 v[48:51], v[0:7], v[168:175], v[48:51]
	v_mfma_f32_16x16x128_f8f6f4 v[40:43], v[8:15], v[168:175], v[200:203]
	v_mfma_f32_16x16x128_f8f6f4 v[32:35], v[0:7], v[176:183], v[204:207]
	v_mfma_f32_16x16x128_f8f6f4 v[24:27], v[8:15], v[176:183], v[216:219]
	v_mfma_f32_16x16x128_f8f6f4 v[16:19], v[0:7], v[184:191], v[220:223]
	v_mfma_f32_16x16x128_f8f6f4 v[8:11], v[8:15], v[184:191], v[224:227]
	v_mfma_f32_16x16x128_f8f6f4 v[52:55], v[144:151], v[160:167], v[52:55]
	v_mfma_f32_16x16x128_f8f6f4 v[44:47], v[152:159], v[160:167], v[228:231]
	v_mfma_f32_16x16x128_f8f6f4 v[36:39], v[144:151], v[168:175], v[232:235]
	v_mfma_f32_16x16x128_f8f6f4 v[28:31], v[152:159], v[168:175], v[236:239]
	v_mfma_f32_16x16x128_f8f6f4 v[20:23], v[144:151], v[176:183], v[240:243]
	v_mfma_f32_16x16x128_f8f6f4 v[12:15], v[152:159], v[176:183], v[244:247]
	v_mfma_f32_16x16x128_f8f6f4 v[4:7], v[144:151], v[184:191], v[248:251]
	v_mfma_f32_16x16x128_f8f6f4 v[0:3], v[152:159], v[184:191], v[132:135]
	s_barrier
	s_setprio 0
	s_add_i32 s86, s86, 2
	s_add_u32 s23, s23, 0x100
	s_addc_u32 s85, s85, 0
	s_cmp_gt_u32 s86, 53
	s_mov_b64 s[24:25], s[26:27]
	s_cbranch_scc0 .LBB0_2007
	s_and_b64 vcc, exec, s[8:9]
	s_cbranch_vccz .LBB0_2010
	s_barrier
